# P6 merge GEMM mid-K rescale: gate loads double-buffered (next group's 4 loads in flight while current group is rescaled)
# speedup vs baseline: 1.0085x; 1.0085x over previous
.LBB0_971:
	s_cmp_lg_u32 s71, 2
	s_cselect_b64 s[40:41], -1, 0
	s_and_b64 s[40:41], s[40:41], s[36:37]
	s_andn2_b64 vcc, exec, s[40:41]
	s_cbranch_vccnz .LBB0_964
	s_cmp_eq_u32 s71, 0
	v_mov_b32_e32 v3, v134
	v_mov_b64_e32 v[136:137], s[8:9]
	s_cselect_b64 vcc, -1, 0
	s_and_b64 s[40:41], vcc, exec
	v_mad_i64_i32 v[4:5], s[42:43], v3, s64, v[136:137]
	v_lshl_add_u64 v[234:235], v[4:5], 0, s[16:17]
	v_lshlrev_b64 v[166:167], 1, v[148:149]
	s_cselect_b32 s0, 0, 0x800
	v_lshl_add_u64 v[4:5], v[234:235], 0, v[166:167]
	s_cselect_b32 s40, 0x800, s63
	s_mov_b32 s41, s1
	v_lshl_add_u64 v[226:227], v[4:5], 0, s[0:1]
	v_lshl_add_u64 v[4:5], v[4:5], 0, s[40:41]
	global_load_dwordx4 v[226:229], v[226:227], off
	s_nop 0
	global_load_dwordx4 v[230:233], v[4:5], off
	v_lshl_add_u64 v[236:237], v[234:235], 0, s[0:1]
	v_lshlrev_b64 v[4:5], 1, v[150:151]
	v_lshl_add_u64 v[234:235], v[234:235], 0, s[40:41]
	v_lshl_add_u64 v[236:237], v[236:237], 0, v[4:5]
	v_lshl_add_u64 v[238:239], v[234:235], 0, v[4:5]
	global_load_dwordx4 v[234:237], v[236:237], off
	s_nop 0
	global_load_dwordx4 v[238:241], v[238:239], off
	v_mov_b32_e32 v3, v164
	s_nop 0
	v_mad_i64_i32 v[168:169], s[42:43], v3, s64, v[136:137]
	v_lshl_add_u64 v[180:181], v[168:169], 0, s[16:17]
	v_lshl_add_u64 v[168:169], v[180:181], 0, v[166:167]
	v_lshl_add_u64 v[170:171], v[168:169], 0, s[0:1]
	v_lshl_add_u64 v[176:177], v[168:169], 0, s[40:41]
	global_load_dwordx4 v[168:171], v[170:171], off
	s_nop 0
	global_load_dwordx4 v[176:179], v[176:177], off
	v_lshl_add_u64 v[184:185], v[180:181], 0, s[0:1]
	v_lshl_add_u64 v[180:181], v[180:181], 0, s[40:41]
	v_lshl_add_u64 v[180:181], v[180:181], 0, v[4:5]
	global_load_dwordx4 v[180:183], v[180:181], off
	v_lshl_add_u64 v[184:185], v[184:185], 0, v[4:5]
	global_load_dwordx4 v[184:187], v[184:185], off
	s_waitcnt vmcnt(4)
	v_cvt_f32_f16_e32 v3, v226
	v_cvt_f32_f16_e32 v135, v230
	v_cvt_f32_f16_sdwa v155, v230 dst_sel:DWORD dst_unused:UNUSED_PAD src0_sel:WORD_1
	v_cvt_f32_f16_e32 v159, v231
	v_cvt_f32_f16_sdwa v153, v226 dst_sel:DWORD dst_unused:UNUSED_PAD src0_sel:WORD_1
	v_max_f32_e32 v135, 0x38d1b717, v135
	v_rcp_f32_e32 v135, v135
	v_cvt_f32_f16_e32 v157, v227
	v_max_f32_e32 v188, 0x38d1b717, v3
	v_max_f32_e32 v155, 0x38d1b717, v155
	v_max_f32_e32 v159, 0x38d1b717, v159
	v_cndmask_b32_e32 v3, v188, v3, vcc
	v_rcp_f32_e32 v155, v155
	v_cvt_f32_f16_sdwa v163, v231 dst_sel:DWORD dst_unused:UNUSED_PAD src0_sel:WORD_1
	v_cvt_f32_f16_e32 v230, v233
	v_cvt_f32_f16_sdwa v231, v233 dst_sel:DWORD dst_unused:UNUSED_PAD src0_sel:WORD_1
	v_cvt_f32_f16_e32 v233, v238
	v_cvt_f32_f16_sdwa v238, v238 dst_sel:DWORD dst_unused:UNUSED_PAD src0_sel:WORD_1
	v_rcp_f32_e32 v159, v159
	v_mul_f32_e32 v3, v3, v135
	v_max_f32_e32 v189, 0x38d1b717, v153
	v_mul_f32_e32 v130, v130, v3
	v_cvt_f32_f16_sdwa v3, v234 dst_sel:DWORD dst_unused:UNUSED_PAD src0_sel:WORD_1
	v_max_f32_e32 v190, 0x38d1b717, v157
	v_cndmask_b32_e32 v153, v189, v153, vcc
	v_cndmask_b32_e32 v157, v190, v157, vcc
	v_mul_f32_e32 v135, v153, v155
	v_mul_f32_e32 v153, v157, v159
	v_mul_f32_e32 v131, v131, v135
	v_max_f32_e32 v135, 0x38d1b717, v238
	v_mul_f32_e32 v132, v132, v153
	v_rcp_f32_e32 v135, v135
	v_max_f32_e32 v153, 0x38d1b717, v3
	v_cndmask_b32_e32 v3, v153, v3, vcc
	v_cvt_f32_f16_e32 v153, v239
	v_mul_f32_e32 v3, v3, v135
	v_cvt_f32_f16_e32 v135, v235
	v_mul_f32_e32 v123, v123, v3
	v_max_f32_e32 v3, 0x38d1b717, v153
	v_rcp_f32_e32 v3, v3
	v_max_f32_e32 v153, 0x38d1b717, v135
	v_cndmask_b32_e32 v135, v153, v135, vcc
	v_cvt_f32_f16_sdwa v153, v239 dst_sel:DWORD dst_unused:UNUSED_PAD src0_sel:WORD_1
	v_mul_f32_e32 v3, v135, v3
	v_cvt_f32_f16_sdwa v135, v235 dst_sel:DWORD dst_unused:UNUSED_PAD src0_sel:WORD_1
	v_mul_f32_e32 v124, v124, v3
	v_max_f32_e32 v3, 0x38d1b717, v153
	v_rcp_f32_e32 v3, v3
	v_max_f32_e32 v153, 0x38d1b717, v135
	v_cndmask_b32_e32 v135, v153, v135, vcc
	v_cvt_f32_f16_e32 v153, v240
	v_mul_f32_e32 v3, v135, v3
	v_cvt_f32_f16_e32 v135, v236
	v_mul_f32_e32 v125, v125, v3
	v_max_f32_e32 v3, 0x38d1b717, v153
	v_rcp_f32_e32 v3, v3
	v_max_f32_e32 v153, 0x38d1b717, v135
	v_cndmask_b32_e32 v135, v153, v135, vcc
	v_cvt_f32_f16_sdwa v153, v240 dst_sel:DWORD dst_unused:UNUSED_PAD src0_sel:WORD_1
	v_mul_f32_e32 v3, v135, v3
	v_cvt_f32_f16_sdwa v135, v236 dst_sel:DWORD dst_unused:UNUSED_PAD src0_sel:WORD_1
	v_mul_f32_e32 v118, v118, v3
	v_max_f32_e32 v3, 0x38d1b717, v153
	v_cvt_f32_f16_sdwa v161, v227 dst_sel:DWORD dst_unused:UNUSED_PAD src0_sel:WORD_1
	v_rcp_f32_e32 v3, v3
	v_max_f32_e32 v153, 0x38d1b717, v135
	v_max_f32_e32 v163, 0x38d1b717, v163
	v_cndmask_b32_e32 v135, v153, v135, vcc
	v_cvt_f32_f16_e32 v153, v241
	v_rcp_f32_e32 v163, v163
	v_max_f32_e32 v191, 0x38d1b717, v161
	v_mul_f32_e32 v3, v135, v3
	v_cvt_f32_f16_e32 v135, v237
	v_cndmask_b32_e32 v161, v191, v161, vcc
	v_mul_f32_e32 v119, v119, v3
	v_max_f32_e32 v3, 0x38d1b717, v153
	v_mul_f32_e32 v155, v161, v163
	v_rcp_f32_e32 v3, v3
	v_cvt_f32_f16_e32 v165, v228
	v_cvt_f32_f16_e32 v226, v232
	v_cvt_f32_f16_sdwa v227, v228 dst_sel:DWORD dst_unused:UNUSED_PAD src0_sel:WORD_1
	v_cvt_f32_f16_sdwa v228, v232 dst_sel:DWORD dst_unused:UNUSED_PAD src0_sel:WORD_1
	v_mul_f32_e32 v133, v133, v155
	v_cvt_f32_f16_sdwa v155, v241 dst_sel:DWORD dst_unused:UNUSED_PAD src0_sel:WORD_1
	v_max_f32_e32 v153, 0x38d1b717, v135
	v_cndmask_b32_e32 v135, v153, v135, vcc
	v_cvt_f32_f16_e32 v175, v229
	v_cvt_f32_f16_sdwa v229, v229 dst_sel:DWORD dst_unused:UNUSED_PAD src0_sel:WORD_1
	v_cvt_f32_f16_e32 v232, v234
	v_mul_f32_e32 v3, v135, v3
	v_cvt_f32_f16_sdwa v135, v237 dst_sel:DWORD dst_unused:UNUSED_PAD src0_sel:WORD_1
	v_max_f32_e32 v226, 0x38d1b717, v226
	v_max_f32_e32 v228, 0x38d1b717, v228
	v_max_f32_e32 v230, 0x38d1b717, v230
	v_max_f32_e32 v231, 0x38d1b717, v231
	v_max_f32_e32 v233, 0x38d1b717, v233
	v_max_f32_e32 v153, 0x38d1b717, v155
	v_rcp_f32_e32 v226, v226
	v_rcp_f32_e32 v228, v228
	v_rcp_f32_e32 v230, v230
	v_rcp_f32_e32 v231, v231
	v_rcp_f32_e32 v233, v233
	v_rcp_f32_e32 v153, v153
	v_max_f32_e32 v192, 0x38d1b717, v165
	v_max_f32_e32 v193, 0x38d1b717, v227
	v_max_f32_e32 v194, 0x38d1b717, v175
	v_max_f32_e32 v195, 0x38d1b717, v229
	v_max_f32_e32 v196, 0x38d1b717, v232
	v_mul_f32_e32 v120, v120, v3
	v_max_f32_e32 v3, 0x38d1b717, v135
	v_cndmask_b32_e32 v165, v192, v165, vcc
	v_cndmask_b32_e32 v227, v193, v227, vcc
	v_cndmask_b32_e32 v175, v194, v175, vcc
	v_cndmask_b32_e32 v229, v195, v229, vcc
	v_cndmask_b32_e32 v232, v196, v232, vcc
	v_cndmask_b32_e32 v3, v3, v135, vcc
	v_mul_f32_e32 v157, v165, v226
	v_mul_f32_e32 v159, v227, v228
	v_mul_f32_e32 v161, v175, v230
	v_mul_f32_e32 v163, v229, v231
	v_mul_f32_e32 v165, v232, v233
	v_mul_f32_e32 v3, v3, v153
	v_mul_f32_e32 v126, v126, v157
	v_mul_f32_e32 v127, v127, v159
	v_mul_f32_e32 v128, v128, v161
	v_mul_f32_e32 v129, v129, v163
	v_mul_f32_e32 v122, v122, v165
	v_mul_f32_e32 v121, v121, v3
	v_mov_b32_e32 v3, v162
	s_nop 0
	v_mad_i64_i32 v[226:227], s[42:43], v3, s64, v[136:137]
	v_lshl_add_u64 v[234:235], v[226:227], 0, s[16:17]
	v_lshl_add_u64 v[230:231], v[234:235], 0, v[166:167]
	v_lshl_add_u64 v[226:227], v[230:231], 0, s[40:41]
	global_load_dwordx4 v[226:229], v[226:227], off
	v_lshl_add_u64 v[230:231], v[230:231], 0, s[0:1]
	global_load_dwordx4 v[230:233], v[230:231], off
	v_lshl_add_u64 v[238:239], v[234:235], 0, s[0:1]
	v_lshl_add_u64 v[234:235], v[234:235], 0, s[40:41]
	v_lshl_add_u64 v[234:235], v[234:235], 0, v[4:5]
	global_load_dwordx4 v[234:237], v[234:235], off
	v_lshl_add_u64 v[238:239], v[238:239], 0, v[4:5]
	global_load_dwordx4 v[238:241], v[238:239], off
	s_waitcnt vmcnt(4)
	v_cvt_f32_f16_e32 v3, v168
	v_cvt_f32_f16_e32 v135, v176
	v_cvt_f32_f16_sdwa v155, v176 dst_sel:DWORD dst_unused:UNUSED_PAD src0_sel:WORD_1
	v_cvt_f32_f16_sdwa v153, v168 dst_sel:DWORD dst_unused:UNUSED_PAD src0_sel:WORD_1
	v_cvt_f32_f16_e32 v159, v177
	v_max_f32_e32 v135, 0x38d1b717, v135
	v_max_f32_e32 v155, 0x38d1b717, v155
	v_rcp_f32_e32 v135, v135
	v_rcp_f32_e32 v155, v155
	v_cvt_f32_f16_e32 v157, v169
	v_max_f32_e32 v163, 0x38d1b717, v3
	v_max_f32_e32 v165, 0x38d1b717, v153
	v_max_f32_e32 v159, 0x38d1b717, v159
	v_cndmask_b32_e32 v3, v163, v3, vcc
	v_cndmask_b32_e32 v153, v165, v153, vcc
	v_rcp_f32_e32 v159, v159
	v_cvt_f32_f16_sdwa v161, v177 dst_sel:DWORD dst_unused:UNUSED_PAD src0_sel:WORD_1
	v_mul_f32_e32 v3, v3, v135
	v_mul_f32_e32 v135, v153, v155
	v_max_f32_e32 v168, 0x38d1b717, v157
	v_mul_f32_e32 v115, v115, v135
	v_cvt_f32_f16_sdwa v135, v169 dst_sel:DWORD dst_unused:UNUSED_PAD src0_sel:WORD_1
	v_cndmask_b32_e32 v157, v168, v157, vcc
	v_mul_f32_e32 v114, v114, v3
	v_mul_f32_e32 v3, v157, v159
	v_mul_f32_e32 v116, v116, v3
	v_max_f32_e32 v3, 0x38d1b717, v161
	v_rcp_f32_e32 v3, v3
	v_max_f32_e32 v153, 0x38d1b717, v135
	v_cndmask_b32_e32 v135, v153, v135, vcc
	v_cvt_f32_f16_e32 v153, v178
	v_mul_f32_e32 v3, v135, v3
	v_cvt_f32_f16_e32 v135, v170
	v_mul_f32_e32 v117, v117, v3
	v_max_f32_e32 v3, 0x38d1b717, v153
	v_rcp_f32_e32 v3, v3
	v_max_f32_e32 v153, 0x38d1b717, v135
	v_cndmask_b32_e32 v135, v153, v135, vcc
	v_cvt_f32_f16_sdwa v153, v178 dst_sel:DWORD dst_unused:UNUSED_PAD src0_sel:WORD_1
	v_mul_f32_e32 v3, v135, v3
	v_cvt_f32_f16_sdwa v135, v170 dst_sel:DWORD dst_unused:UNUSED_PAD src0_sel:WORD_1
	v_mul_f32_e32 v110, v110, v3
	v_max_f32_e32 v3, 0x38d1b717, v153
	v_rcp_f32_e32 v3, v3
	v_max_f32_e32 v153, 0x38d1b717, v135
	v_cndmask_b32_e32 v135, v153, v135, vcc
	v_cvt_f32_f16_e32 v153, v179
	v_mul_f32_e32 v3, v135, v3
	v_cvt_f32_f16_e32 v135, v171
	v_mul_f32_e32 v111, v111, v3
	v_max_f32_e32 v3, 0x38d1b717, v153
	v_rcp_f32_e32 v3, v3
	v_max_f32_e32 v153, 0x38d1b717, v135
	v_cndmask_b32_e32 v135, v153, v135, vcc
	v_cvt_f32_f16_sdwa v153, v179 dst_sel:DWORD dst_unused:UNUSED_PAD src0_sel:WORD_1
	v_mul_f32_e32 v3, v135, v3
	v_cvt_f32_f16_sdwa v135, v171 dst_sel:DWORD dst_unused:UNUSED_PAD src0_sel:WORD_1
	v_mul_f32_e32 v112, v112, v3
	v_max_f32_e32 v3, 0x38d1b717, v153
	v_rcp_f32_e32 v3, v3
	v_max_f32_e32 v153, 0x38d1b717, v135
	v_cndmask_b32_e32 v135, v153, v135, vcc
	v_cvt_f32_f16_e32 v153, v180
	v_mul_f32_e32 v3, v135, v3
	v_cvt_f32_f16_e32 v135, v184
	v_mul_f32_e32 v113, v113, v3
	v_max_f32_e32 v3, 0x38d1b717, v153
	v_rcp_f32_e32 v3, v3
	v_max_f32_e32 v153, 0x38d1b717, v135
	v_cndmask_b32_e32 v135, v153, v135, vcc
	v_cvt_f32_f16_sdwa v153, v180 dst_sel:DWORD dst_unused:UNUSED_PAD src0_sel:WORD_1
	v_mul_f32_e32 v3, v135, v3
	v_cvt_f32_f16_sdwa v135, v184 dst_sel:DWORD dst_unused:UNUSED_PAD src0_sel:WORD_1
	v_mul_f32_e32 v106, v106, v3
	v_max_f32_e32 v3, 0x38d1b717, v153
	v_rcp_f32_e32 v3, v3
	v_max_f32_e32 v153, 0x38d1b717, v135
	v_cndmask_b32_e32 v135, v153, v135, vcc
	v_cvt_f32_f16_e32 v153, v181
	v_mul_f32_e32 v3, v135, v3
	v_cvt_f32_f16_e32 v135, v185
	v_mul_f32_e32 v107, v107, v3
	v_max_f32_e32 v3, 0x38d1b717, v153
	v_rcp_f32_e32 v3, v3
	v_max_f32_e32 v153, 0x38d1b717, v135
	v_cndmask_b32_e32 v135, v153, v135, vcc
	v_cvt_f32_f16_sdwa v153, v181 dst_sel:DWORD dst_unused:UNUSED_PAD src0_sel:WORD_1
	v_mul_f32_e32 v3, v135, v3
	v_cvt_f32_f16_sdwa v135, v185 dst_sel:DWORD dst_unused:UNUSED_PAD src0_sel:WORD_1
	v_mul_f32_e32 v108, v108, v3
	v_max_f32_e32 v3, 0x38d1b717, v153
	v_rcp_f32_e32 v3, v3
	v_max_f32_e32 v153, 0x38d1b717, v135
	v_cndmask_b32_e32 v135, v153, v135, vcc
	v_cvt_f32_f16_e32 v153, v182
	v_mul_f32_e32 v3, v135, v3
	v_cvt_f32_f16_e32 v135, v186
	v_mul_f32_e32 v109, v109, v3
	v_max_f32_e32 v3, 0x38d1b717, v153
	v_rcp_f32_e32 v3, v3
	v_max_f32_e32 v153, 0x38d1b717, v135
	v_cndmask_b32_e32 v135, v153, v135, vcc
	v_cvt_f32_f16_sdwa v153, v182 dst_sel:DWORD dst_unused:UNUSED_PAD src0_sel:WORD_1
	v_mul_f32_e32 v3, v135, v3
	v_cvt_f32_f16_sdwa v135, v186 dst_sel:DWORD dst_unused:UNUSED_PAD src0_sel:WORD_1
	v_mul_f32_e32 v102, v102, v3
	v_max_f32_e32 v3, 0x38d1b717, v153
	v_rcp_f32_e32 v3, v3
	v_max_f32_e32 v153, 0x38d1b717, v135
	v_cndmask_b32_e32 v135, v153, v135, vcc
	v_cvt_f32_f16_e32 v153, v183
	v_mul_f32_e32 v3, v135, v3
	v_cvt_f32_f16_e32 v135, v187
	v_mul_f32_e32 v103, v103, v3
	v_max_f32_e32 v3, 0x38d1b717, v153
	v_rcp_f32_e32 v3, v3
	v_cvt_f32_f16_sdwa v155, v183 dst_sel:DWORD dst_unused:UNUSED_PAD src0_sel:WORD_1
	v_max_f32_e32 v153, 0x38d1b717, v135
	v_cndmask_b32_e32 v135, v153, v135, vcc
	v_mul_f32_e32 v3, v135, v3
	v_cvt_f32_f16_sdwa v135, v187 dst_sel:DWORD dst_unused:UNUSED_PAD src0_sel:WORD_1
	v_max_f32_e32 v153, 0x38d1b717, v155
	v_rcp_f32_e32 v153, v153
	v_mul_f32_e32 v104, v104, v3
	v_max_f32_e32 v3, 0x38d1b717, v135
	v_cndmask_b32_e32 v3, v3, v135, vcc
	v_mul_f32_e32 v3, v3, v153
	v_mul_f32_e32 v105, v105, v3
	v_mov_b32_e32 v3, v160
	s_nop 0
	v_mad_i64_i32 v[168:169], s[42:43], v3, s64, v[136:137]
	v_lshl_add_u64 v[180:181], v[168:169], 0, s[16:17]
	v_lshl_add_u64 v[176:177], v[180:181], 0, v[166:167]
	v_lshl_add_u64 v[168:169], v[176:177], 0, s[40:41]
	global_load_dwordx4 v[168:171], v[168:169], off
	v_lshl_add_u64 v[176:177], v[176:177], 0, s[0:1]
	global_load_dwordx4 v[176:179], v[176:177], off
	v_lshl_add_u64 v[184:185], v[180:181], 0, s[0:1]
	v_lshl_add_u64 v[180:181], v[180:181], 0, s[40:41]
	v_lshl_add_u64 v[180:181], v[180:181], 0, v[4:5]
	global_load_dwordx4 v[180:183], v[180:181], off
	v_lshl_add_u64 v[184:185], v[184:185], 0, v[4:5]
	global_load_dwordx4 v[184:187], v[184:185], off
	s_waitcnt vmcnt(4)
	v_cvt_f32_f16_e32 v3, v226
	v_cvt_f32_f16_e32 v135, v230
	v_max_f32_e32 v3, 0x38d1b717, v3
	v_rcp_f32_e32 v3, v3
	v_max_f32_e32 v153, 0x38d1b717, v135
	v_cndmask_b32_e32 v135, v153, v135, vcc
	v_cvt_f32_f16_sdwa v153, v226 dst_sel:DWORD dst_unused:UNUSED_PAD src0_sel:WORD_1
	v_mul_f32_e32 v3, v135, v3
	v_cvt_f32_f16_sdwa v135, v230 dst_sel:DWORD dst_unused:UNUSED_PAD src0_sel:WORD_1
	v_mul_f32_e32 v98, v98, v3
	v_max_f32_e32 v3, 0x38d1b717, v153
	v_rcp_f32_e32 v3, v3
	v_max_f32_e32 v153, 0x38d1b717, v135
	v_cndmask_b32_e32 v135, v153, v135, vcc
	v_cvt_f32_f16_e32 v153, v227
	v_mul_f32_e32 v3, v135, v3
	v_cvt_f32_f16_e32 v135, v231
	v_mul_f32_e32 v99, v99, v3
	v_max_f32_e32 v3, 0x38d1b717, v153
	v_rcp_f32_e32 v3, v3
	v_max_f32_e32 v153, 0x38d1b717, v135
	v_cndmask_b32_e32 v135, v153, v135, vcc
	v_cvt_f32_f16_sdwa v153, v227 dst_sel:DWORD dst_unused:UNUSED_PAD src0_sel:WORD_1
	v_mul_f32_e32 v3, v135, v3
	v_cvt_f32_f16_sdwa v135, v231 dst_sel:DWORD dst_unused:UNUSED_PAD src0_sel:WORD_1
	v_mul_f32_e32 v100, v100, v3
	v_max_f32_e32 v3, 0x38d1b717, v153
	v_rcp_f32_e32 v3, v3
	v_max_f32_e32 v153, 0x38d1b717, v135
	v_cndmask_b32_e32 v135, v153, v135, vcc
	v_cvt_f32_f16_e32 v153, v228
	v_mul_f32_e32 v3, v135, v3
	v_cvt_f32_f16_e32 v135, v232
	v_mul_f32_e32 v101, v101, v3
	v_max_f32_e32 v3, 0x38d1b717, v153
	v_rcp_f32_e32 v3, v3
	v_max_f32_e32 v153, 0x38d1b717, v135
	v_cndmask_b32_e32 v135, v153, v135, vcc
	v_cvt_f32_f16_sdwa v153, v228 dst_sel:DWORD dst_unused:UNUSED_PAD src0_sel:WORD_1
	v_mul_f32_e32 v3, v135, v3
	v_cvt_f32_f16_sdwa v135, v232 dst_sel:DWORD dst_unused:UNUSED_PAD src0_sel:WORD_1
	v_mul_f32_e32 v94, v94, v3
	v_max_f32_e32 v3, 0x38d1b717, v153
	v_rcp_f32_e32 v3, v3
	v_max_f32_e32 v153, 0x38d1b717, v135
	v_cndmask_b32_e32 v135, v153, v135, vcc
	v_cvt_f32_f16_e32 v153, v229
	v_mul_f32_e32 v3, v135, v3
	v_cvt_f32_f16_e32 v135, v233
	v_mul_f32_e32 v95, v95, v3
	v_max_f32_e32 v3, 0x38d1b717, v153
	v_rcp_f32_e32 v3, v3
	v_max_f32_e32 v153, 0x38d1b717, v135
	v_cndmask_b32_e32 v135, v153, v135, vcc
	v_cvt_f32_f16_sdwa v153, v229 dst_sel:DWORD dst_unused:UNUSED_PAD src0_sel:WORD_1
	v_mul_f32_e32 v3, v135, v3
	v_cvt_f32_f16_sdwa v135, v233 dst_sel:DWORD dst_unused:UNUSED_PAD src0_sel:WORD_1
	v_mul_f32_e32 v96, v96, v3
	v_max_f32_e32 v3, 0x38d1b717, v153
	v_rcp_f32_e32 v3, v3
	v_max_f32_e32 v153, 0x38d1b717, v135
	v_cndmask_b32_e32 v135, v153, v135, vcc
	v_cvt_f32_f16_e32 v153, v234
	v_mul_f32_e32 v3, v135, v3
	v_cvt_f32_f16_e32 v135, v238
	v_mul_f32_e32 v97, v97, v3
	v_max_f32_e32 v3, 0x38d1b717, v153
	v_rcp_f32_e32 v3, v3
	v_max_f32_e32 v153, 0x38d1b717, v135
	v_cndmask_b32_e32 v135, v153, v135, vcc
	v_cvt_f32_f16_sdwa v153, v234 dst_sel:DWORD dst_unused:UNUSED_PAD src0_sel:WORD_1
	v_mul_f32_e32 v3, v135, v3
	v_cvt_f32_f16_sdwa v135, v238 dst_sel:DWORD dst_unused:UNUSED_PAD src0_sel:WORD_1
	v_mul_f32_e32 v90, v90, v3
	v_max_f32_e32 v3, 0x38d1b717, v153
	v_rcp_f32_e32 v3, v3
	v_max_f32_e32 v153, 0x38d1b717, v135
	v_cndmask_b32_e32 v135, v153, v135, vcc
	v_cvt_f32_f16_e32 v153, v235
	v_mul_f32_e32 v3, v135, v3
	v_cvt_f32_f16_e32 v135, v239
	v_mul_f32_e32 v91, v91, v3
	v_max_f32_e32 v3, 0x38d1b717, v153
	v_rcp_f32_e32 v3, v3
	v_max_f32_e32 v153, 0x38d1b717, v135
	v_cndmask_b32_e32 v135, v153, v135, vcc
	v_cvt_f32_f16_sdwa v153, v235 dst_sel:DWORD dst_unused:UNUSED_PAD src0_sel:WORD_1
	v_mul_f32_e32 v3, v135, v3
	v_cvt_f32_f16_sdwa v135, v239 dst_sel:DWORD dst_unused:UNUSED_PAD src0_sel:WORD_1
	v_mul_f32_e32 v92, v92, v3
	v_max_f32_e32 v3, 0x38d1b717, v153
	v_rcp_f32_e32 v3, v3
	v_max_f32_e32 v153, 0x38d1b717, v135
	v_cndmask_b32_e32 v135, v153, v135, vcc
	v_cvt_f32_f16_e32 v153, v236
	v_mul_f32_e32 v3, v135, v3
	v_cvt_f32_f16_e32 v135, v240
	v_mul_f32_e32 v93, v93, v3
	v_max_f32_e32 v3, 0x38d1b717, v153
	v_rcp_f32_e32 v3, v3
	v_max_f32_e32 v153, 0x38d1b717, v135
	v_cndmask_b32_e32 v135, v153, v135, vcc
	v_cvt_f32_f16_sdwa v153, v236 dst_sel:DWORD dst_unused:UNUSED_PAD src0_sel:WORD_1
	v_mul_f32_e32 v3, v135, v3
	v_cvt_f32_f16_sdwa v135, v240 dst_sel:DWORD dst_unused:UNUSED_PAD src0_sel:WORD_1
	v_mul_f32_e32 v86, v86, v3
	v_max_f32_e32 v3, 0x38d1b717, v153
	v_rcp_f32_e32 v3, v3
	v_max_f32_e32 v153, 0x38d1b717, v135
	v_cndmask_b32_e32 v135, v153, v135, vcc
	v_cvt_f32_f16_e32 v153, v237
	v_mul_f32_e32 v3, v135, v3
	v_cvt_f32_f16_e32 v135, v241
	v_mul_f32_e32 v87, v87, v3
	v_max_f32_e32 v3, 0x38d1b717, v153
	v_rcp_f32_e32 v3, v3
	v_cvt_f32_f16_sdwa v155, v237 dst_sel:DWORD dst_unused:UNUSED_PAD src0_sel:WORD_1
	v_max_f32_e32 v153, 0x38d1b717, v135
	v_cndmask_b32_e32 v135, v153, v135, vcc
	v_mul_f32_e32 v3, v135, v3
	v_cvt_f32_f16_sdwa v135, v241 dst_sel:DWORD dst_unused:UNUSED_PAD src0_sel:WORD_1
	v_max_f32_e32 v153, 0x38d1b717, v155
	v_rcp_f32_e32 v153, v153
	v_mul_f32_e32 v88, v88, v3
	v_max_f32_e32 v3, 0x38d1b717, v135
	v_cndmask_b32_e32 v3, v3, v135, vcc
	v_mul_f32_e32 v3, v3, v153
	v_mul_f32_e32 v89, v89, v3
	v_mov_b32_e32 v3, v158
	s_nop 0
	v_mad_i64_i32 v[226:227], s[42:43], v3, s64, v[136:137]
	v_lshl_add_u64 v[234:235], v[226:227], 0, s[16:17]
	v_lshl_add_u64 v[230:231], v[234:235], 0, v[166:167]
	v_lshl_add_u64 v[226:227], v[230:231], 0, s[40:41]
	global_load_dwordx4 v[226:229], v[226:227], off
	v_lshl_add_u64 v[230:231], v[230:231], 0, s[0:1]
	global_load_dwordx4 v[230:233], v[230:231], off
	v_lshl_add_u64 v[238:239], v[234:235], 0, s[0:1]
	v_lshl_add_u64 v[234:235], v[234:235], 0, s[40:41]
	v_lshl_add_u64 v[234:235], v[234:235], 0, v[4:5]
	global_load_dwordx4 v[234:237], v[234:235], off
	v_lshl_add_u64 v[238:239], v[238:239], 0, v[4:5]
	global_load_dwordx4 v[238:241], v[238:239], off
	s_waitcnt vmcnt(4)
	v_cvt_f32_f16_e32 v3, v168
	v_cvt_f32_f16_e32 v135, v176
	v_max_f32_e32 v3, 0x38d1b717, v3
	v_rcp_f32_e32 v3, v3
	v_max_f32_e32 v153, 0x38d1b717, v135
	v_cndmask_b32_e32 v135, v153, v135, vcc
	v_cvt_f32_f16_sdwa v153, v168 dst_sel:DWORD dst_unused:UNUSED_PAD src0_sel:WORD_1
	v_mul_f32_e32 v3, v135, v3
	v_cvt_f32_f16_sdwa v135, v176 dst_sel:DWORD dst_unused:UNUSED_PAD src0_sel:WORD_1
	v_mul_f32_e32 v82, v82, v3
	v_max_f32_e32 v3, 0x38d1b717, v153
	v_rcp_f32_e32 v3, v3
	v_max_f32_e32 v153, 0x38d1b717, v135
	v_cndmask_b32_e32 v135, v153, v135, vcc
	v_cvt_f32_f16_e32 v153, v169
	v_mul_f32_e32 v3, v135, v3
	v_cvt_f32_f16_e32 v135, v177
	v_mul_f32_e32 v83, v83, v3
	v_max_f32_e32 v3, 0x38d1b717, v153
	v_rcp_f32_e32 v3, v3
	v_max_f32_e32 v153, 0x38d1b717, v135
	v_cndmask_b32_e32 v135, v153, v135, vcc
	v_cvt_f32_f16_sdwa v153, v169 dst_sel:DWORD dst_unused:UNUSED_PAD src0_sel:WORD_1
	v_mul_f32_e32 v3, v135, v3
	v_cvt_f32_f16_sdwa v135, v177 dst_sel:DWORD dst_unused:UNUSED_PAD src0_sel:WORD_1
	v_mul_f32_e32 v84, v84, v3
	v_max_f32_e32 v3, 0x38d1b717, v153
	v_rcp_f32_e32 v3, v3
	v_max_f32_e32 v153, 0x38d1b717, v135
	v_cndmask_b32_e32 v135, v153, v135, vcc
	v_cvt_f32_f16_e32 v153, v170
	v_mul_f32_e32 v3, v135, v3
	v_cvt_f32_f16_e32 v135, v178
	v_mul_f32_e32 v85, v85, v3
	v_max_f32_e32 v3, 0x38d1b717, v153
	v_rcp_f32_e32 v3, v3
	v_max_f32_e32 v153, 0x38d1b717, v135
	v_cndmask_b32_e32 v135, v153, v135, vcc
	v_cvt_f32_f16_sdwa v153, v170 dst_sel:DWORD dst_unused:UNUSED_PAD src0_sel:WORD_1
	v_mul_f32_e32 v3, v135, v3
	v_cvt_f32_f16_sdwa v135, v178 dst_sel:DWORD dst_unused:UNUSED_PAD src0_sel:WORD_1
	v_mul_f32_e32 v78, v78, v3
	v_max_f32_e32 v3, 0x38d1b717, v153
	v_rcp_f32_e32 v3, v3
	v_max_f32_e32 v153, 0x38d1b717, v135
	v_cndmask_b32_e32 v135, v153, v135, vcc
	v_cvt_f32_f16_e32 v153, v171
	v_mul_f32_e32 v3, v135, v3
	v_cvt_f32_f16_e32 v135, v179
	v_mul_f32_e32 v79, v79, v3
	v_max_f32_e32 v3, 0x38d1b717, v153
	v_rcp_f32_e32 v3, v3
	v_max_f32_e32 v153, 0x38d1b717, v135
	v_cndmask_b32_e32 v135, v153, v135, vcc
	v_cvt_f32_f16_sdwa v153, v171 dst_sel:DWORD dst_unused:UNUSED_PAD src0_sel:WORD_1
	v_mul_f32_e32 v3, v135, v3
	v_cvt_f32_f16_sdwa v135, v179 dst_sel:DWORD dst_unused:UNUSED_PAD src0_sel:WORD_1
	v_mul_f32_e32 v80, v80, v3
	v_max_f32_e32 v3, 0x38d1b717, v153
	v_rcp_f32_e32 v3, v3
	v_max_f32_e32 v153, 0x38d1b717, v135
	v_cndmask_b32_e32 v135, v153, v135, vcc
	v_cvt_f32_f16_e32 v153, v180
	v_mul_f32_e32 v3, v135, v3
	v_cvt_f32_f16_e32 v135, v184
	v_mul_f32_e32 v81, v81, v3
	v_max_f32_e32 v3, 0x38d1b717, v153
	v_rcp_f32_e32 v3, v3
	v_max_f32_e32 v153, 0x38d1b717, v135
	v_cndmask_b32_e32 v135, v153, v135, vcc
	v_cvt_f32_f16_sdwa v153, v180 dst_sel:DWORD dst_unused:UNUSED_PAD src0_sel:WORD_1
	v_mul_f32_e32 v3, v135, v3
	v_cvt_f32_f16_sdwa v135, v184 dst_sel:DWORD dst_unused:UNUSED_PAD src0_sel:WORD_1
	v_mul_f32_e32 v74, v74, v3
	v_max_f32_e32 v3, 0x38d1b717, v153
	v_rcp_f32_e32 v3, v3
	v_max_f32_e32 v153, 0x38d1b717, v135
	v_cndmask_b32_e32 v135, v153, v135, vcc
	v_cvt_f32_f16_e32 v153, v181
	v_mul_f32_e32 v3, v135, v3
	v_cvt_f32_f16_e32 v135, v185
	v_mul_f32_e32 v75, v75, v3
	v_max_f32_e32 v3, 0x38d1b717, v153
	v_rcp_f32_e32 v3, v3
	v_max_f32_e32 v153, 0x38d1b717, v135
	v_cndmask_b32_e32 v135, v153, v135, vcc
	v_cvt_f32_f16_sdwa v153, v181 dst_sel:DWORD dst_unused:UNUSED_PAD src0_sel:WORD_1
	v_mul_f32_e32 v3, v135, v3
	v_cvt_f32_f16_sdwa v135, v185 dst_sel:DWORD dst_unused:UNUSED_PAD src0_sel:WORD_1
	v_mul_f32_e32 v76, v76, v3
	v_max_f32_e32 v3, 0x38d1b717, v153
	v_rcp_f32_e32 v3, v3
	v_max_f32_e32 v153, 0x38d1b717, v135
	v_cndmask_b32_e32 v135, v153, v135, vcc
	v_cvt_f32_f16_e32 v153, v182
	v_mul_f32_e32 v3, v135, v3
	v_cvt_f32_f16_e32 v135, v186
	v_mul_f32_e32 v77, v77, v3
	v_max_f32_e32 v3, 0x38d1b717, v153
	v_rcp_f32_e32 v3, v3
	v_max_f32_e32 v153, 0x38d1b717, v135
	v_cndmask_b32_e32 v135, v153, v135, vcc
	v_cvt_f32_f16_sdwa v153, v182 dst_sel:DWORD dst_unused:UNUSED_PAD src0_sel:WORD_1
	v_mul_f32_e32 v3, v135, v3
	v_cvt_f32_f16_sdwa v135, v186 dst_sel:DWORD dst_unused:UNUSED_PAD src0_sel:WORD_1
	v_mul_f32_e32 v70, v70, v3
	v_max_f32_e32 v3, 0x38d1b717, v153
	v_rcp_f32_e32 v3, v3
	v_max_f32_e32 v153, 0x38d1b717, v135
	v_cndmask_b32_e32 v135, v153, v135, vcc
	v_cvt_f32_f16_e32 v153, v183
	v_mul_f32_e32 v3, v135, v3
	v_cvt_f32_f16_e32 v135, v187
	v_mul_f32_e32 v71, v71, v3
	v_max_f32_e32 v3, 0x38d1b717, v153
	v_rcp_f32_e32 v3, v3
	v_cvt_f32_f16_sdwa v155, v183 dst_sel:DWORD dst_unused:UNUSED_PAD src0_sel:WORD_1
	v_max_f32_e32 v153, 0x38d1b717, v135
	v_cndmask_b32_e32 v135, v153, v135, vcc
	v_mul_f32_e32 v3, v135, v3
	v_cvt_f32_f16_sdwa v135, v187 dst_sel:DWORD dst_unused:UNUSED_PAD src0_sel:WORD_1
	v_max_f32_e32 v153, 0x38d1b717, v155
	v_rcp_f32_e32 v153, v153
	v_mul_f32_e32 v72, v72, v3
	v_max_f32_e32 v3, 0x38d1b717, v135
	v_cndmask_b32_e32 v3, v3, v135, vcc
	v_mul_f32_e32 v3, v3, v153
	v_mul_f32_e32 v73, v73, v3
	v_mov_b32_e32 v3, v156
	s_nop 0
	v_mad_i64_i32 v[168:169], s[42:43], v3, s64, v[136:137]
	v_lshl_add_u64 v[180:181], v[168:169], 0, s[16:17]
	v_lshl_add_u64 v[176:177], v[180:181], 0, v[166:167]
	v_lshl_add_u64 v[168:169], v[176:177], 0, s[40:41]
	global_load_dwordx4 v[168:171], v[168:169], off
	v_lshl_add_u64 v[176:177], v[176:177], 0, s[0:1]
	global_load_dwordx4 v[176:179], v[176:177], off
	v_lshl_add_u64 v[184:185], v[180:181], 0, s[0:1]
	v_lshl_add_u64 v[180:181], v[180:181], 0, s[40:41]
	v_lshl_add_u64 v[180:181], v[180:181], 0, v[4:5]
	global_load_dwordx4 v[180:183], v[180:181], off
	v_lshl_add_u64 v[184:185], v[184:185], 0, v[4:5]
	global_load_dwordx4 v[184:187], v[184:185], off
	s_waitcnt vmcnt(4)
	v_cvt_f32_f16_e32 v3, v226
	v_cvt_f32_f16_e32 v135, v230
	v_max_f32_e32 v3, 0x38d1b717, v3
	v_rcp_f32_e32 v3, v3
	v_max_f32_e32 v153, 0x38d1b717, v135
	v_cndmask_b32_e32 v135, v153, v135, vcc
	v_cvt_f32_f16_sdwa v153, v226 dst_sel:DWORD dst_unused:UNUSED_PAD src0_sel:WORD_1
	v_mul_f32_e32 v3, v135, v3
	v_cvt_f32_f16_sdwa v135, v230 dst_sel:DWORD dst_unused:UNUSED_PAD src0_sel:WORD_1
	v_mul_f32_e32 v66, v66, v3
	v_max_f32_e32 v3, 0x38d1b717, v153
	v_rcp_f32_e32 v3, v3
	v_max_f32_e32 v153, 0x38d1b717, v135
	v_cndmask_b32_e32 v135, v153, v135, vcc
	v_cvt_f32_f16_e32 v153, v227
	v_mul_f32_e32 v3, v135, v3
	v_cvt_f32_f16_e32 v135, v231
	v_mul_f32_e32 v67, v67, v3
	v_max_f32_e32 v3, 0x38d1b717, v153
	v_rcp_f32_e32 v3, v3
	v_max_f32_e32 v153, 0x38d1b717, v135
	v_cndmask_b32_e32 v135, v153, v135, vcc
	v_cvt_f32_f16_sdwa v153, v227 dst_sel:DWORD dst_unused:UNUSED_PAD src0_sel:WORD_1
	v_mul_f32_e32 v3, v135, v3
	v_cvt_f32_f16_sdwa v135, v231 dst_sel:DWORD dst_unused:UNUSED_PAD src0_sel:WORD_1
	v_mul_f32_e32 v68, v68, v3
	v_max_f32_e32 v3, 0x38d1b717, v153
	v_rcp_f32_e32 v3, v3
	v_max_f32_e32 v153, 0x38d1b717, v135
	v_cndmask_b32_e32 v135, v153, v135, vcc
	v_cvt_f32_f16_e32 v153, v228
	v_mul_f32_e32 v3, v135, v3
	v_cvt_f32_f16_e32 v135, v232
	v_mul_f32_e32 v69, v69, v3
	v_max_f32_e32 v3, 0x38d1b717, v153
	v_rcp_f32_e32 v3, v3
	v_max_f32_e32 v153, 0x38d1b717, v135
	v_cndmask_b32_e32 v135, v153, v135, vcc
	v_cvt_f32_f16_sdwa v153, v228 dst_sel:DWORD dst_unused:UNUSED_PAD src0_sel:WORD_1
	v_mul_f32_e32 v3, v135, v3
	v_cvt_f32_f16_sdwa v135, v232 dst_sel:DWORD dst_unused:UNUSED_PAD src0_sel:WORD_1
	v_mul_f32_e32 v62, v62, v3
	v_max_f32_e32 v3, 0x38d1b717, v153
	v_rcp_f32_e32 v3, v3
	v_max_f32_e32 v153, 0x38d1b717, v135
	v_cndmask_b32_e32 v135, v153, v135, vcc
	v_cvt_f32_f16_e32 v153, v229
	v_mul_f32_e32 v3, v135, v3
	v_cvt_f32_f16_e32 v135, v233
	v_mul_f32_e32 v63, v63, v3
	v_max_f32_e32 v3, 0x38d1b717, v153
	v_rcp_f32_e32 v3, v3
	v_max_f32_e32 v153, 0x38d1b717, v135
	v_cndmask_b32_e32 v135, v153, v135, vcc
	v_cvt_f32_f16_sdwa v153, v229 dst_sel:DWORD dst_unused:UNUSED_PAD src0_sel:WORD_1
	v_mul_f32_e32 v3, v135, v3
	v_cvt_f32_f16_sdwa v135, v233 dst_sel:DWORD dst_unused:UNUSED_PAD src0_sel:WORD_1
	v_mul_f32_e32 v64, v64, v3
	v_max_f32_e32 v3, 0x38d1b717, v153
	v_rcp_f32_e32 v3, v3
	v_max_f32_e32 v153, 0x38d1b717, v135
	v_cndmask_b32_e32 v135, v153, v135, vcc
	v_cvt_f32_f16_e32 v153, v234
	v_mul_f32_e32 v3, v135, v3
	v_cvt_f32_f16_e32 v135, v238
	v_mul_f32_e32 v65, v65, v3
	v_max_f32_e32 v3, 0x38d1b717, v153
	v_rcp_f32_e32 v3, v3
	v_max_f32_e32 v153, 0x38d1b717, v135
	v_cndmask_b32_e32 v135, v153, v135, vcc
	v_cvt_f32_f16_sdwa v153, v234 dst_sel:DWORD dst_unused:UNUSED_PAD src0_sel:WORD_1
	v_mul_f32_e32 v3, v135, v3
	v_cvt_f32_f16_sdwa v135, v238 dst_sel:DWORD dst_unused:UNUSED_PAD src0_sel:WORD_1
	v_mul_f32_e32 v58, v58, v3
	v_max_f32_e32 v3, 0x38d1b717, v153
	v_rcp_f32_e32 v3, v3
	v_max_f32_e32 v153, 0x38d1b717, v135
	v_cndmask_b32_e32 v135, v153, v135, vcc
	v_cvt_f32_f16_e32 v153, v235
	v_mul_f32_e32 v3, v135, v3
	v_cvt_f32_f16_e32 v135, v239
	v_mul_f32_e32 v59, v59, v3
	v_max_f32_e32 v3, 0x38d1b717, v153
	v_rcp_f32_e32 v3, v3
	v_max_f32_e32 v153, 0x38d1b717, v135
	v_cndmask_b32_e32 v135, v153, v135, vcc
	v_cvt_f32_f16_sdwa v153, v235 dst_sel:DWORD dst_unused:UNUSED_PAD src0_sel:WORD_1
	v_mul_f32_e32 v3, v135, v3
	v_cvt_f32_f16_sdwa v135, v239 dst_sel:DWORD dst_unused:UNUSED_PAD src0_sel:WORD_1
	v_mul_f32_e32 v60, v60, v3
	v_max_f32_e32 v3, 0x38d1b717, v153
	v_rcp_f32_e32 v3, v3
	v_max_f32_e32 v153, 0x38d1b717, v135
	v_cndmask_b32_e32 v135, v153, v135, vcc
	v_cvt_f32_f16_e32 v153, v236
	v_mul_f32_e32 v3, v135, v3
	v_cvt_f32_f16_e32 v135, v240
	v_mul_f32_e32 v61, v61, v3
	v_max_f32_e32 v3, 0x38d1b717, v153
	v_rcp_f32_e32 v3, v3
	v_max_f32_e32 v153, 0x38d1b717, v135
	v_cndmask_b32_e32 v135, v153, v135, vcc
	v_cvt_f32_f16_sdwa v153, v236 dst_sel:DWORD dst_unused:UNUSED_PAD src0_sel:WORD_1
	v_mul_f32_e32 v3, v135, v3
	v_cvt_f32_f16_sdwa v135, v240 dst_sel:DWORD dst_unused:UNUSED_PAD src0_sel:WORD_1
	v_mul_f32_e32 v54, v54, v3
	v_max_f32_e32 v3, 0x38d1b717, v153
	v_rcp_f32_e32 v3, v3
	v_max_f32_e32 v153, 0x38d1b717, v135
	v_cndmask_b32_e32 v135, v153, v135, vcc
	v_cvt_f32_f16_e32 v153, v237
	v_mul_f32_e32 v3, v135, v3
	v_cvt_f32_f16_e32 v135, v241
	v_mul_f32_e32 v55, v55, v3
	v_max_f32_e32 v3, 0x38d1b717, v153
	v_rcp_f32_e32 v3, v3
	v_cvt_f32_f16_sdwa v155, v237 dst_sel:DWORD dst_unused:UNUSED_PAD src0_sel:WORD_1
	v_max_f32_e32 v153, 0x38d1b717, v135
	v_cndmask_b32_e32 v135, v153, v135, vcc
	v_mul_f32_e32 v3, v135, v3
	v_cvt_f32_f16_sdwa v135, v241 dst_sel:DWORD dst_unused:UNUSED_PAD src0_sel:WORD_1
	v_max_f32_e32 v153, 0x38d1b717, v155
	v_rcp_f32_e32 v153, v153
	v_mul_f32_e32 v56, v56, v3
	v_max_f32_e32 v3, 0x38d1b717, v135
	v_cndmask_b32_e32 v3, v3, v135, vcc
	v_mul_f32_e32 v3, v3, v153
	v_mul_f32_e32 v57, v57, v3
	v_mov_b32_e32 v3, v154
	s_nop 0
	v_mad_i64_i32 v[226:227], s[42:43], v3, s64, v[136:137]
	v_lshl_add_u64 v[234:235], v[226:227], 0, s[16:17]
	v_lshl_add_u64 v[230:231], v[234:235], 0, v[166:167]
	v_lshl_add_u64 v[226:227], v[230:231], 0, s[40:41]
	global_load_dwordx4 v[226:229], v[226:227], off
	v_lshl_add_u64 v[230:231], v[230:231], 0, s[0:1]
	global_load_dwordx4 v[230:233], v[230:231], off
	v_lshl_add_u64 v[238:239], v[234:235], 0, s[0:1]
	v_lshl_add_u64 v[234:235], v[234:235], 0, s[40:41]
	v_lshl_add_u64 v[234:235], v[234:235], 0, v[4:5]
	global_load_dwordx4 v[234:237], v[234:235], off
	v_lshl_add_u64 v[238:239], v[238:239], 0, v[4:5]
	global_load_dwordx4 v[238:241], v[238:239], off
	s_waitcnt vmcnt(4)
	v_cvt_f32_f16_e32 v3, v168
	v_cvt_f32_f16_e32 v135, v176
	v_max_f32_e32 v3, 0x38d1b717, v3
	v_rcp_f32_e32 v3, v3
	v_max_f32_e32 v153, 0x38d1b717, v135
	v_cndmask_b32_e32 v135, v153, v135, vcc
	v_cvt_f32_f16_sdwa v153, v168 dst_sel:DWORD dst_unused:UNUSED_PAD src0_sel:WORD_1
	v_mul_f32_e32 v3, v135, v3
	v_cvt_f32_f16_sdwa v135, v176 dst_sel:DWORD dst_unused:UNUSED_PAD src0_sel:WORD_1
	v_mul_f32_e32 v50, v50, v3
	v_max_f32_e32 v3, 0x38d1b717, v153
	v_rcp_f32_e32 v3, v3
	v_max_f32_e32 v153, 0x38d1b717, v135
	v_cndmask_b32_e32 v135, v153, v135, vcc
	v_cvt_f32_f16_e32 v153, v169
	v_mul_f32_e32 v3, v135, v3
	v_cvt_f32_f16_e32 v135, v177
	v_mul_f32_e32 v51, v51, v3
	v_max_f32_e32 v3, 0x38d1b717, v153
	v_rcp_f32_e32 v3, v3
	v_max_f32_e32 v153, 0x38d1b717, v135
	v_cndmask_b32_e32 v135, v153, v135, vcc
	v_cvt_f32_f16_sdwa v153, v169 dst_sel:DWORD dst_unused:UNUSED_PAD src0_sel:WORD_1
	v_mul_f32_e32 v3, v135, v3
	v_cvt_f32_f16_sdwa v135, v177 dst_sel:DWORD dst_unused:UNUSED_PAD src0_sel:WORD_1
	v_mul_f32_e32 v52, v52, v3
	v_max_f32_e32 v3, 0x38d1b717, v153
	v_rcp_f32_e32 v3, v3
	v_max_f32_e32 v153, 0x38d1b717, v135
	v_cndmask_b32_e32 v135, v153, v135, vcc
	v_cvt_f32_f16_e32 v153, v170
	v_mul_f32_e32 v3, v135, v3
	v_cvt_f32_f16_e32 v135, v178
	v_mul_f32_e32 v53, v53, v3
	v_max_f32_e32 v3, 0x38d1b717, v153
	v_rcp_f32_e32 v3, v3
	v_max_f32_e32 v153, 0x38d1b717, v135
	v_cndmask_b32_e32 v135, v153, v135, vcc
	v_cvt_f32_f16_sdwa v153, v170 dst_sel:DWORD dst_unused:UNUSED_PAD src0_sel:WORD_1
	v_mul_f32_e32 v3, v135, v3
	v_cvt_f32_f16_sdwa v135, v178 dst_sel:DWORD dst_unused:UNUSED_PAD src0_sel:WORD_1
	v_mul_f32_e32 v46, v46, v3
	v_max_f32_e32 v3, 0x38d1b717, v153
	v_rcp_f32_e32 v3, v3
	v_max_f32_e32 v153, 0x38d1b717, v135
	v_cndmask_b32_e32 v135, v153, v135, vcc
	v_cvt_f32_f16_e32 v153, v171
	v_mul_f32_e32 v3, v135, v3
	v_cvt_f32_f16_e32 v135, v179
	v_mul_f32_e32 v47, v47, v3
	v_max_f32_e32 v3, 0x38d1b717, v153
	v_rcp_f32_e32 v3, v3
	v_max_f32_e32 v153, 0x38d1b717, v135
	v_cndmask_b32_e32 v135, v153, v135, vcc
	v_cvt_f32_f16_sdwa v153, v171 dst_sel:DWORD dst_unused:UNUSED_PAD src0_sel:WORD_1
	v_mul_f32_e32 v3, v135, v3
	v_cvt_f32_f16_sdwa v135, v179 dst_sel:DWORD dst_unused:UNUSED_PAD src0_sel:WORD_1
	v_mul_f32_e32 v48, v48, v3
	v_max_f32_e32 v3, 0x38d1b717, v153
	v_rcp_f32_e32 v3, v3
	v_max_f32_e32 v153, 0x38d1b717, v135
	v_cndmask_b32_e32 v135, v153, v135, vcc
	v_cvt_f32_f16_e32 v153, v180
	v_mul_f32_e32 v3, v135, v3
	v_cvt_f32_f16_e32 v135, v184
	v_mul_f32_e32 v49, v49, v3
	v_max_f32_e32 v3, 0x38d1b717, v153
	v_rcp_f32_e32 v3, v3
	v_max_f32_e32 v153, 0x38d1b717, v135
	v_cndmask_b32_e32 v135, v153, v135, vcc
	v_cvt_f32_f16_sdwa v153, v180 dst_sel:DWORD dst_unused:UNUSED_PAD src0_sel:WORD_1
	v_mul_f32_e32 v3, v135, v3
	v_cvt_f32_f16_sdwa v135, v184 dst_sel:DWORD dst_unused:UNUSED_PAD src0_sel:WORD_1
	v_mul_f32_e32 v42, v42, v3
	v_max_f32_e32 v3, 0x38d1b717, v153
	v_rcp_f32_e32 v3, v3
	v_max_f32_e32 v153, 0x38d1b717, v135
	v_cndmask_b32_e32 v135, v153, v135, vcc
	v_cvt_f32_f16_e32 v153, v181
	v_mul_f32_e32 v3, v135, v3
	v_cvt_f32_f16_e32 v135, v185
	v_mul_f32_e32 v43, v43, v3
	v_max_f32_e32 v3, 0x38d1b717, v153
	v_rcp_f32_e32 v3, v3
	v_max_f32_e32 v153, 0x38d1b717, v135
	v_cndmask_b32_e32 v135, v153, v135, vcc
	v_cvt_f32_f16_sdwa v153, v181 dst_sel:DWORD dst_unused:UNUSED_PAD src0_sel:WORD_1
	v_mul_f32_e32 v3, v135, v3
	v_cvt_f32_f16_sdwa v135, v185 dst_sel:DWORD dst_unused:UNUSED_PAD src0_sel:WORD_1
	v_mul_f32_e32 v44, v44, v3
	v_max_f32_e32 v3, 0x38d1b717, v153
	v_rcp_f32_e32 v3, v3
	v_max_f32_e32 v153, 0x38d1b717, v135
	v_cndmask_b32_e32 v135, v153, v135, vcc
	v_cvt_f32_f16_e32 v153, v182
	v_mul_f32_e32 v3, v135, v3
	v_cvt_f32_f16_e32 v135, v186
	v_mul_f32_e32 v45, v45, v3
	v_max_f32_e32 v3, 0x38d1b717, v153
	v_rcp_f32_e32 v3, v3
	v_max_f32_e32 v153, 0x38d1b717, v135
	v_cndmask_b32_e32 v135, v153, v135, vcc
	v_cvt_f32_f16_sdwa v153, v182 dst_sel:DWORD dst_unused:UNUSED_PAD src0_sel:WORD_1
	v_mul_f32_e32 v3, v135, v3
	v_cvt_f32_f16_sdwa v135, v186 dst_sel:DWORD dst_unused:UNUSED_PAD src0_sel:WORD_1
	v_mul_f32_e32 v38, v38, v3
	v_max_f32_e32 v3, 0x38d1b717, v153
	v_rcp_f32_e32 v3, v3
	v_max_f32_e32 v153, 0x38d1b717, v135
	v_cndmask_b32_e32 v135, v153, v135, vcc
	v_cvt_f32_f16_e32 v153, v183
	v_mul_f32_e32 v3, v135, v3
	v_cvt_f32_f16_e32 v135, v187
	v_mul_f32_e32 v39, v39, v3
	v_max_f32_e32 v3, 0x38d1b717, v153
	v_rcp_f32_e32 v3, v3
	v_cvt_f32_f16_sdwa v155, v183 dst_sel:DWORD dst_unused:UNUSED_PAD src0_sel:WORD_1
	v_max_f32_e32 v153, 0x38d1b717, v135
	v_cndmask_b32_e32 v135, v153, v135, vcc
	v_mul_f32_e32 v3, v135, v3
	v_cvt_f32_f16_sdwa v135, v187 dst_sel:DWORD dst_unused:UNUSED_PAD src0_sel:WORD_1
	v_max_f32_e32 v153, 0x38d1b717, v155
	v_rcp_f32_e32 v153, v153
	v_mul_f32_e32 v40, v40, v3
	v_max_f32_e32 v3, 0x38d1b717, v135
	v_cndmask_b32_e32 v3, v3, v135, vcc
	v_mul_f32_e32 v3, v3, v153
	v_mul_f32_e32 v41, v41, v3
	v_mov_b32_e32 v3, v152
	s_nop 0
	v_mad_i64_i32 v[136:137], s[42:43], v3, s64, v[136:137]
	v_lshl_add_u64 v[136:137], v[136:137], 0, s[16:17]
	v_lshl_add_u64 v[170:171], v[136:137], 0, v[166:167]
	v_lshl_add_u64 v[166:167], v[170:171], 0, s[40:41]
	global_load_dwordx4 v[166:169], v[166:167], off
	v_lshl_add_u64 v[170:171], v[170:171], 0, s[0:1]
	global_load_dwordx4 v[176:179], v[170:171], off
	v_lshl_add_u64 v[170:171], v[136:137], 0, s[0:1]
	v_lshl_add_u64 v[136:137], v[136:137], 0, s[40:41]
	v_lshl_add_u64 v[136:137], v[136:137], 0, v[4:5]
	global_load_dwordx4 v[180:183], v[136:137], off
	v_lshl_add_u64 v[4:5], v[170:171], 0, v[4:5]
	global_load_dwordx4 v[184:187], v[4:5], off
	s_waitcnt vmcnt(4)
	v_cvt_f32_f16_e32 v3, v226
	v_cvt_f32_f16_e32 v135, v230
	v_max_f32_e32 v3, 0x38d1b717, v3
	v_rcp_f32_e32 v3, v3
	v_max_f32_e32 v153, 0x38d1b717, v135
	v_cndmask_b32_e32 v135, v153, v135, vcc
	v_cvt_f32_f16_sdwa v153, v226 dst_sel:DWORD dst_unused:UNUSED_PAD src0_sel:WORD_1
	v_mul_f32_e32 v3, v135, v3
	v_cvt_f32_f16_sdwa v135, v230 dst_sel:DWORD dst_unused:UNUSED_PAD src0_sel:WORD_1
	v_mul_f32_e32 v34, v34, v3
	v_max_f32_e32 v3, 0x38d1b717, v153
	v_rcp_f32_e32 v3, v3
	v_max_f32_e32 v153, 0x38d1b717, v135
	v_cndmask_b32_e32 v135, v153, v135, vcc
	v_cvt_f32_f16_e32 v153, v227
	v_mul_f32_e32 v3, v135, v3
	v_cvt_f32_f16_e32 v135, v231
	v_mul_f32_e32 v35, v35, v3
	v_max_f32_e32 v3, 0x38d1b717, v153
	v_rcp_f32_e32 v3, v3
	v_max_f32_e32 v153, 0x38d1b717, v135
	v_cndmask_b32_e32 v135, v153, v135, vcc
	v_cvt_f32_f16_sdwa v153, v227 dst_sel:DWORD dst_unused:UNUSED_PAD src0_sel:WORD_1
	v_mul_f32_e32 v3, v135, v3
	v_cvt_f32_f16_sdwa v135, v231 dst_sel:DWORD dst_unused:UNUSED_PAD src0_sel:WORD_1
	v_mul_f32_e32 v36, v36, v3
	v_max_f32_e32 v3, 0x38d1b717, v153
	v_rcp_f32_e32 v3, v3
	v_max_f32_e32 v153, 0x38d1b717, v135
	v_cndmask_b32_e32 v135, v153, v135, vcc
	v_cvt_f32_f16_e32 v153, v228
	v_mul_f32_e32 v3, v135, v3
	v_cvt_f32_f16_e32 v135, v232
	v_mul_f32_e32 v37, v37, v3
	v_max_f32_e32 v3, 0x38d1b717, v153
	v_rcp_f32_e32 v3, v3
	v_max_f32_e32 v153, 0x38d1b717, v135
	v_cndmask_b32_e32 v135, v153, v135, vcc
	v_cvt_f32_f16_sdwa v153, v228 dst_sel:DWORD dst_unused:UNUSED_PAD src0_sel:WORD_1
	v_mul_f32_e32 v3, v135, v3
	v_cvt_f32_f16_sdwa v135, v232 dst_sel:DWORD dst_unused:UNUSED_PAD src0_sel:WORD_1
	v_mul_f32_e32 v30, v30, v3
	v_max_f32_e32 v3, 0x38d1b717, v153
	v_rcp_f32_e32 v3, v3
	v_max_f32_e32 v153, 0x38d1b717, v135
	v_cndmask_b32_e32 v135, v153, v135, vcc
	v_cvt_f32_f16_e32 v153, v229
	v_mul_f32_e32 v3, v135, v3
	v_cvt_f32_f16_e32 v135, v233
	v_mul_f32_e32 v31, v31, v3
	v_max_f32_e32 v3, 0x38d1b717, v153
	v_rcp_f32_e32 v3, v3
	v_max_f32_e32 v153, 0x38d1b717, v135
	v_cndmask_b32_e32 v135, v153, v135, vcc
	v_cvt_f32_f16_sdwa v153, v229 dst_sel:DWORD dst_unused:UNUSED_PAD src0_sel:WORD_1
	v_mul_f32_e32 v3, v135, v3
	v_cvt_f32_f16_sdwa v135, v233 dst_sel:DWORD dst_unused:UNUSED_PAD src0_sel:WORD_1
	v_mul_f32_e32 v32, v32, v3
	v_max_f32_e32 v3, 0x38d1b717, v153
	v_rcp_f32_e32 v3, v3
	v_max_f32_e32 v153, 0x38d1b717, v135
	v_cndmask_b32_e32 v135, v153, v135, vcc
	v_cvt_f32_f16_e32 v153, v234
	v_mul_f32_e32 v3, v135, v3
	v_cvt_f32_f16_e32 v135, v238
	v_mul_f32_e32 v33, v33, v3
	v_max_f32_e32 v3, 0x38d1b717, v153
	v_rcp_f32_e32 v3, v3
	v_max_f32_e32 v153, 0x38d1b717, v135
	v_cndmask_b32_e32 v135, v153, v135, vcc
	v_cvt_f32_f16_sdwa v153, v234 dst_sel:DWORD dst_unused:UNUSED_PAD src0_sel:WORD_1
	v_mul_f32_e32 v3, v135, v3
	v_cvt_f32_f16_sdwa v135, v238 dst_sel:DWORD dst_unused:UNUSED_PAD src0_sel:WORD_1
	v_mul_f32_e32 v26, v26, v3
	v_max_f32_e32 v3, 0x38d1b717, v153
	v_rcp_f32_e32 v3, v3
	v_max_f32_e32 v153, 0x38d1b717, v135
	v_cndmask_b32_e32 v135, v153, v135, vcc
	v_cvt_f32_f16_e32 v153, v235
	v_mul_f32_e32 v3, v135, v3
	v_cvt_f32_f16_e32 v135, v239
	v_mul_f32_e32 v27, v27, v3
	v_max_f32_e32 v3, 0x38d1b717, v153
	v_rcp_f32_e32 v3, v3
	v_max_f32_e32 v153, 0x38d1b717, v135
	v_cndmask_b32_e32 v135, v153, v135, vcc
	v_cvt_f32_f16_sdwa v153, v235 dst_sel:DWORD dst_unused:UNUSED_PAD src0_sel:WORD_1
	v_mul_f32_e32 v3, v135, v3
	v_cvt_f32_f16_sdwa v135, v239 dst_sel:DWORD dst_unused:UNUSED_PAD src0_sel:WORD_1
	v_mul_f32_e32 v28, v28, v3
	v_max_f32_e32 v3, 0x38d1b717, v153
	v_rcp_f32_e32 v3, v3
	v_max_f32_e32 v153, 0x38d1b717, v135
	v_cndmask_b32_e32 v135, v153, v135, vcc
	v_cvt_f32_f16_e32 v153, v236
	v_mul_f32_e32 v3, v135, v3
	v_cvt_f32_f16_e32 v135, v240
	v_mul_f32_e32 v29, v29, v3
	v_max_f32_e32 v3, 0x38d1b717, v153
	v_rcp_f32_e32 v3, v3
	v_max_f32_e32 v153, 0x38d1b717, v135
	v_cndmask_b32_e32 v135, v153, v135, vcc
	v_cvt_f32_f16_sdwa v153, v236 dst_sel:DWORD dst_unused:UNUSED_PAD src0_sel:WORD_1
	v_mul_f32_e32 v3, v135, v3
	v_cvt_f32_f16_sdwa v135, v240 dst_sel:DWORD dst_unused:UNUSED_PAD src0_sel:WORD_1
	v_mul_f32_e32 v22, v22, v3
	v_max_f32_e32 v3, 0x38d1b717, v153
	v_rcp_f32_e32 v3, v3
	v_max_f32_e32 v153, 0x38d1b717, v135
	v_cndmask_b32_e32 v135, v153, v135, vcc
	v_cvt_f32_f16_e32 v153, v237
	v_mul_f32_e32 v3, v135, v3
	v_cvt_f32_f16_e32 v135, v241
	v_mul_f32_e32 v23, v23, v3
	v_max_f32_e32 v3, 0x38d1b717, v153
	v_rcp_f32_e32 v3, v3
	v_cvt_f32_f16_sdwa v155, v237 dst_sel:DWORD dst_unused:UNUSED_PAD src0_sel:WORD_1
	v_max_f32_e32 v153, 0x38d1b717, v135
	v_cndmask_b32_e32 v135, v153, v135, vcc
	v_mul_f32_e32 v3, v135, v3
	v_cvt_f32_f16_sdwa v135, v241 dst_sel:DWORD dst_unused:UNUSED_PAD src0_sel:WORD_1
	v_max_f32_e32 v153, 0x38d1b717, v155
	v_rcp_f32_e32 v153, v153
	v_mul_f32_e32 v24, v24, v3
	v_max_f32_e32 v3, 0x38d1b717, v135
	v_cndmask_b32_e32 v3, v3, v135, vcc
	v_mul_f32_e32 v3, v3, v153
	v_mul_f32_e32 v25, v25, v3
	s_waitcnt vmcnt(0)
	v_cvt_f32_f16_e32 v3, v166
	v_cvt_f32_f16_e32 v4, v176
	v_max_f32_e32 v3, 0x38d1b717, v3
	v_rcp_f32_e32 v3, v3
	v_max_f32_e32 v5, 0x38d1b717, v4
	v_cndmask_b32_e32 v4, v5, v4, vcc
	v_cvt_f32_f16_sdwa v5, v166 dst_sel:DWORD dst_unused:UNUSED_PAD src0_sel:WORD_1
	v_mul_f32_e32 v3, v4, v3
	v_cvt_f32_f16_sdwa v4, v176 dst_sel:DWORD dst_unused:UNUSED_PAD src0_sel:WORD_1
	v_mul_f32_e32 v18, v18, v3
	v_max_f32_e32 v3, 0x38d1b717, v5
	v_rcp_f32_e32 v3, v3
	v_max_f32_e32 v5, 0x38d1b717, v4
	v_cndmask_b32_e32 v4, v5, v4, vcc
	v_cvt_f32_f16_e32 v5, v167
	v_mul_f32_e32 v3, v4, v3
	v_cvt_f32_f16_e32 v4, v177
	v_mul_f32_e32 v19, v19, v3
	v_max_f32_e32 v3, 0x38d1b717, v5
	v_rcp_f32_e32 v3, v3
	v_max_f32_e32 v5, 0x38d1b717, v4
	v_cndmask_b32_e32 v4, v5, v4, vcc
	v_cvt_f32_f16_sdwa v5, v167 dst_sel:DWORD dst_unused:UNUSED_PAD src0_sel:WORD_1
	v_mul_f32_e32 v3, v4, v3
	v_cvt_f32_f16_sdwa v4, v177 dst_sel:DWORD dst_unused:UNUSED_PAD src0_sel:WORD_1
	v_mul_f32_e32 v20, v20, v3
	v_max_f32_e32 v3, 0x38d1b717, v5
	v_rcp_f32_e32 v3, v3
	v_max_f32_e32 v5, 0x38d1b717, v4
	v_cndmask_b32_e32 v4, v5, v4, vcc
	v_cvt_f32_f16_e32 v5, v168
	v_mul_f32_e32 v3, v4, v3
	v_cvt_f32_f16_e32 v4, v178
	v_mul_f32_e32 v21, v21, v3
	v_max_f32_e32 v3, 0x38d1b717, v5
	v_rcp_f32_e32 v3, v3
	v_max_f32_e32 v5, 0x38d1b717, v4
	v_cndmask_b32_e32 v4, v5, v4, vcc
	v_cvt_f32_f16_sdwa v5, v168 dst_sel:DWORD dst_unused:UNUSED_PAD src0_sel:WORD_1
	v_mul_f32_e32 v3, v4, v3
	v_cvt_f32_f16_sdwa v4, v178 dst_sel:DWORD dst_unused:UNUSED_PAD src0_sel:WORD_1
	v_mul_f32_e32 v14, v14, v3
	v_max_f32_e32 v3, 0x38d1b717, v5
	v_rcp_f32_e32 v3, v3
	v_max_f32_e32 v5, 0x38d1b717, v4
	v_cndmask_b32_e32 v4, v5, v4, vcc
	v_cvt_f32_f16_e32 v5, v169
	v_mul_f32_e32 v3, v4, v3
	v_cvt_f32_f16_e32 v4, v179
	v_mul_f32_e32 v15, v15, v3
	v_max_f32_e32 v3, 0x38d1b717, v5
	v_rcp_f32_e32 v3, v3
	v_max_f32_e32 v5, 0x38d1b717, v4
	v_cndmask_b32_e32 v4, v5, v4, vcc
	v_cvt_f32_f16_sdwa v5, v169 dst_sel:DWORD dst_unused:UNUSED_PAD src0_sel:WORD_1
	v_mul_f32_e32 v3, v4, v3
	v_cvt_f32_f16_sdwa v4, v179 dst_sel:DWORD dst_unused:UNUSED_PAD src0_sel:WORD_1
	v_mul_f32_e32 v16, v16, v3
	v_max_f32_e32 v3, 0x38d1b717, v5
	v_rcp_f32_e32 v3, v3
	v_max_f32_e32 v5, 0x38d1b717, v4
	v_cndmask_b32_e32 v4, v5, v4, vcc
	v_cvt_f32_f16_e32 v5, v180
	v_mul_f32_e32 v3, v4, v3
	v_cvt_f32_f16_e32 v4, v184
	v_mul_f32_e32 v17, v17, v3
	v_max_f32_e32 v3, 0x38d1b717, v5
	v_rcp_f32_e32 v3, v3
	v_max_f32_e32 v5, 0x38d1b717, v4
	v_cndmask_b32_e32 v4, v5, v4, vcc
	v_cvt_f32_f16_sdwa v5, v180 dst_sel:DWORD dst_unused:UNUSED_PAD src0_sel:WORD_1
	v_mul_f32_e32 v3, v4, v3
	v_cvt_f32_f16_sdwa v4, v184 dst_sel:DWORD dst_unused:UNUSED_PAD src0_sel:WORD_1
	v_mul_f32_e32 v10, v10, v3
	v_max_f32_e32 v3, 0x38d1b717, v5
	v_rcp_f32_e32 v3, v3
	v_max_f32_e32 v5, 0x38d1b717, v4
	v_cndmask_b32_e32 v4, v5, v4, vcc
	v_cvt_f32_f16_e32 v5, v181
	v_mul_f32_e32 v3, v4, v3
	v_cvt_f32_f16_e32 v4, v185
	v_mul_f32_e32 v11, v11, v3
	v_max_f32_e32 v3, 0x38d1b717, v5
	v_rcp_f32_e32 v3, v3
	v_max_f32_e32 v5, 0x38d1b717, v4
	v_cndmask_b32_e32 v4, v5, v4, vcc
	v_cvt_f32_f16_sdwa v5, v181 dst_sel:DWORD dst_unused:UNUSED_PAD src0_sel:WORD_1
	v_mul_f32_e32 v3, v4, v3
	v_cvt_f32_f16_sdwa v4, v185 dst_sel:DWORD dst_unused:UNUSED_PAD src0_sel:WORD_1
	v_mul_f32_e32 v12, v12, v3
	v_max_f32_e32 v3, 0x38d1b717, v5
	v_rcp_f32_e32 v3, v3
	v_max_f32_e32 v5, 0x38d1b717, v4
	v_cndmask_b32_e32 v4, v5, v4, vcc
	v_cvt_f32_f16_e32 v5, v182
	v_mul_f32_e32 v3, v4, v3
	v_cvt_f32_f16_e32 v4, v186
	v_mul_f32_e32 v13, v13, v3
	v_max_f32_e32 v3, 0x38d1b717, v5
	v_rcp_f32_e32 v3, v3
	v_max_f32_e32 v5, 0x38d1b717, v4
	v_cndmask_b32_e32 v4, v5, v4, vcc
	v_cvt_f32_f16_sdwa v5, v182 dst_sel:DWORD dst_unused:UNUSED_PAD src0_sel:WORD_1
	v_mul_f32_e32 v3, v4, v3
	v_cvt_f32_f16_sdwa v4, v186 dst_sel:DWORD dst_unused:UNUSED_PAD src0_sel:WORD_1
	v_mul_f32_e32 v6, v6, v3
	v_max_f32_e32 v3, 0x38d1b717, v5
	v_rcp_f32_e32 v3, v3
	v_max_f32_e32 v5, 0x38d1b717, v4
	v_cndmask_b32_e32 v4, v5, v4, vcc
	v_cvt_f32_f16_e32 v5, v183
	v_mul_f32_e32 v3, v4, v3
	v_cvt_f32_f16_e32 v4, v187
	v_mul_f32_e32 v7, v7, v3
	v_max_f32_e32 v3, 0x38d1b717, v5
	v_rcp_f32_e32 v3, v3
	v_cvt_f32_f16_sdwa v135, v183 dst_sel:DWORD dst_unused:UNUSED_PAD src0_sel:WORD_1
	v_max_f32_e32 v5, 0x38d1b717, v4
	v_cndmask_b32_e32 v4, v5, v4, vcc
	v_mul_f32_e32 v3, v4, v3
	v_cvt_f32_f16_sdwa v4, v187 dst_sel:DWORD dst_unused:UNUSED_PAD src0_sel:WORD_1
	v_max_f32_e32 v5, 0x38d1b717, v135
	v_rcp_f32_e32 v5, v5
	v_mul_f32_e32 v8, v8, v3
	v_max_f32_e32 v3, 0x38d1b717, v4
	v_cndmask_b32_e32 v3, v3, v4, vcc
	v_mul_f32_e32 v3, v3, v5
	v_mul_f32_e32 v9, v9, v3
	s_branch .LBB0_964

.LBB0_5355:
	s_cmp_lg_u32 s65, 2
	s_cselect_b64 s[38:39], -1, 0
	s_and_b64 s[38:39], s[38:39], s[34:35]
	s_andn2_b64 vcc, exec, s[38:39]
	s_cbranch_vccnz .LBB0_5351
	v_mov_b32_e32 v3, v134
	v_mov_b64_e32 v[136:137], s[8:9]
	s_and_b64 s[38:39], s[0:1], exec
	v_mad_i64_i32 v[4:5], s[40:41], v3, s62, v[136:137]
	v_lshl_add_u64 v[234:235], v[4:5], 0, s[16:17]
	v_lshlrev_b64 v[166:167], 1, v[148:149]
	s_cselect_b32 s2, 0, 0x800
	v_lshl_add_u64 v[4:5], v[234:235], 0, v[166:167]
	s_cselect_b32 s38, 0x800, s61
	s_mov_b32 s39, s3
	v_lshl_add_u64 v[226:227], v[4:5], 0, s[2:3]
	v_lshl_add_u64 v[4:5], v[4:5], 0, s[38:39]
	global_load_dwordx4 v[226:229], v[226:227], off
	s_nop 0
	global_load_dwordx4 v[230:233], v[4:5], off
	v_lshlrev_b64 v[4:5], 1, v[150:151]
	v_lshl_add_u64 v[236:237], v[234:235], 0, s[2:3]
	v_lshl_add_u64 v[234:235], v[234:235], 0, s[38:39]
	v_lshl_add_u64 v[236:237], v[236:237], 0, v[4:5]
	v_lshl_add_u64 v[238:239], v[234:235], 0, v[4:5]
	global_load_dwordx4 v[234:237], v[236:237], off
	s_nop 0
	global_load_dwordx4 v[238:241], v[238:239], off
	v_mov_b32_e32 v3, v164
	s_nop 0
	v_mad_i64_i32 v[168:169], s[40:41], v3, s62, v[136:137]
	v_lshl_add_u64 v[180:181], v[168:169], 0, s[16:17]
	v_lshl_add_u64 v[168:169], v[180:181], 0, v[166:167]
	v_lshl_add_u64 v[170:171], v[168:169], 0, s[2:3]
	v_lshl_add_u64 v[176:177], v[168:169], 0, s[38:39]
	global_load_dwordx4 v[168:171], v[170:171], off
	s_nop 0
	global_load_dwordx4 v[176:179], v[176:177], off
	v_lshl_add_u64 v[184:185], v[180:181], 0, s[2:3]
	v_lshl_add_u64 v[180:181], v[180:181], 0, s[38:39]
	v_lshl_add_u64 v[180:181], v[180:181], 0, v[4:5]
	global_load_dwordx4 v[180:183], v[180:181], off
	v_lshl_add_u64 v[184:185], v[184:185], 0, v[4:5]
	global_load_dwordx4 v[184:187], v[184:185], off
	s_waitcnt vmcnt(4)
	v_cvt_f32_f16_e32 v3, v226
	v_cvt_f32_f16_e32 v135, v230
	v_cvt_f32_f16_sdwa v155, v230 dst_sel:DWORD dst_unused:UNUSED_PAD src0_sel:WORD_1
	v_cvt_f32_f16_e32 v159, v231
	v_cvt_f32_f16_sdwa v153, v226 dst_sel:DWORD dst_unused:UNUSED_PAD src0_sel:WORD_1
	v_max_f32_e32 v135, 0x38d1b717, v135
	v_cvt_f32_f16_e32 v157, v227
	v_rcp_f32_e32 v135, v135
	v_cvt_f32_f16_sdwa v163, v231 dst_sel:DWORD dst_unused:UNUSED_PAD src0_sel:WORD_1
	v_cvt_f32_f16_e32 v230, v233
	v_cvt_f32_f16_sdwa v231, v233 dst_sel:DWORD dst_unused:UNUSED_PAD src0_sel:WORD_1
	v_cvt_f32_f16_e32 v233, v238
	v_cvt_f32_f16_sdwa v238, v238 dst_sel:DWORD dst_unused:UNUSED_PAD src0_sel:WORD_1
	v_max_f32_e32 v155, 0x38d1b717, v155
	v_max_f32_e32 v159, 0x38d1b717, v159
	v_max_f32_e32 v188, 0x38d1b717, v3
	v_rcp_f32_e32 v155, v155
	v_rcp_f32_e32 v159, v159
	v_cndmask_b32_e64 v3, v188, v3, s[0:1]
	v_cvt_f32_f16_sdwa v161, v227 dst_sel:DWORD dst_unused:UNUSED_PAD src0_sel:WORD_1
	v_cvt_f32_f16_e32 v165, v228
	v_cvt_f32_f16_e32 v226, v232
	v_cvt_f32_f16_sdwa v227, v228 dst_sel:DWORD dst_unused:UNUSED_PAD src0_sel:WORD_1
	v_cvt_f32_f16_sdwa v228, v232 dst_sel:DWORD dst_unused:UNUSED_PAD src0_sel:WORD_1
	v_cvt_f32_f16_e32 v232, v234
	v_cvt_f32_f16_sdwa v234, v234 dst_sel:DWORD dst_unused:UNUSED_PAD src0_sel:WORD_1
	v_max_f32_e32 v189, 0x38d1b717, v153
	v_max_f32_e32 v190, 0x38d1b717, v157
	v_mul_f32_e32 v3, v3, v135
	v_cndmask_b32_e64 v153, v189, v153, s[0:1]
	v_cndmask_b32_e64 v157, v190, v157, s[0:1]
	v_mul_f32_e32 v130, v130, v3
	v_max_f32_e32 v3, 0x38d1b717, v238
	v_mul_f32_e32 v135, v153, v155
	v_mul_f32_e32 v153, v157, v159
	v_rcp_f32_e32 v3, v3
	v_mul_f32_e32 v132, v132, v153
	v_cvt_f32_f16_e32 v153, v239
	v_mul_f32_e32 v131, v131, v135
	v_max_f32_e32 v135, 0x38d1b717, v234
	v_cndmask_b32_e64 v135, v135, v234, s[0:1]
	v_mul_f32_e32 v3, v135, v3
	v_cvt_f32_f16_e32 v135, v235
	v_mul_f32_e32 v123, v123, v3
	v_max_f32_e32 v3, 0x38d1b717, v153
	v_rcp_f32_e32 v3, v3
	v_max_f32_e32 v153, 0x38d1b717, v135
	v_cndmask_b32_e64 v135, v153, v135, s[0:1]
	v_cvt_f32_f16_sdwa v153, v239 dst_sel:DWORD dst_unused:UNUSED_PAD src0_sel:WORD_1
	v_mul_f32_e32 v3, v135, v3
	v_cvt_f32_f16_sdwa v135, v235 dst_sel:DWORD dst_unused:UNUSED_PAD src0_sel:WORD_1
	v_mul_f32_e32 v124, v124, v3
	v_max_f32_e32 v3, 0x38d1b717, v153
	v_rcp_f32_e32 v3, v3
	v_max_f32_e32 v153, 0x38d1b717, v135
	v_cndmask_b32_e64 v135, v153, v135, s[0:1]
	v_cvt_f32_f16_e32 v153, v240
	v_mul_f32_e32 v3, v135, v3
	v_cvt_f32_f16_e32 v135, v236
	v_mul_f32_e32 v125, v125, v3
	v_max_f32_e32 v3, 0x38d1b717, v153
	v_rcp_f32_e32 v3, v3
	v_max_f32_e32 v153, 0x38d1b717, v135
	v_cndmask_b32_e64 v135, v153, v135, s[0:1]
	v_cvt_f32_f16_sdwa v153, v240 dst_sel:DWORD dst_unused:UNUSED_PAD src0_sel:WORD_1
	v_mul_f32_e32 v3, v135, v3
	v_cvt_f32_f16_sdwa v135, v236 dst_sel:DWORD dst_unused:UNUSED_PAD src0_sel:WORD_1
	v_mul_f32_e32 v118, v118, v3
	v_max_f32_e32 v3, 0x38d1b717, v153
	v_rcp_f32_e32 v3, v3
	v_max_f32_e32 v153, 0x38d1b717, v135
	v_max_f32_e32 v163, 0x38d1b717, v163
	v_cndmask_b32_e64 v135, v153, v135, s[0:1]
	v_cvt_f32_f16_e32 v153, v241
	v_rcp_f32_e32 v163, v163
	v_max_f32_e32 v191, 0x38d1b717, v161
	v_mul_f32_e32 v3, v135, v3
	v_cvt_f32_f16_e32 v135, v237
	v_cndmask_b32_e64 v161, v191, v161, s[0:1]
	v_mul_f32_e32 v119, v119, v3
	v_max_f32_e32 v3, 0x38d1b717, v153
	v_mul_f32_e32 v155, v161, v163
	v_rcp_f32_e32 v3, v3
	v_mul_f32_e32 v133, v133, v155
	v_cvt_f32_f16_sdwa v155, v241 dst_sel:DWORD dst_unused:UNUSED_PAD src0_sel:WORD_1
	v_max_f32_e32 v153, 0x38d1b717, v135
	v_cndmask_b32_e64 v135, v153, v135, s[0:1]
	v_cvt_f32_f16_e32 v175, v229
	v_cvt_f32_f16_sdwa v229, v229 dst_sel:DWORD dst_unused:UNUSED_PAD src0_sel:WORD_1
	v_mul_f32_e32 v3, v135, v3
	v_cvt_f32_f16_sdwa v135, v237 dst_sel:DWORD dst_unused:UNUSED_PAD src0_sel:WORD_1
	v_max_f32_e32 v226, 0x38d1b717, v226
	v_max_f32_e32 v228, 0x38d1b717, v228
	v_max_f32_e32 v230, 0x38d1b717, v230
	v_max_f32_e32 v231, 0x38d1b717, v231
	v_max_f32_e32 v233, 0x38d1b717, v233
	v_max_f32_e32 v153, 0x38d1b717, v155
	v_rcp_f32_e32 v226, v226
	v_rcp_f32_e32 v228, v228
	v_rcp_f32_e32 v230, v230
	v_rcp_f32_e32 v231, v231
	v_rcp_f32_e32 v233, v233
	v_rcp_f32_e32 v153, v153
	v_max_f32_e32 v192, 0x38d1b717, v165
	v_max_f32_e32 v193, 0x38d1b717, v227
	v_max_f32_e32 v194, 0x38d1b717, v175
	v_max_f32_e32 v195, 0x38d1b717, v229
	v_max_f32_e32 v196, 0x38d1b717, v232
	v_mul_f32_e32 v120, v120, v3
	v_max_f32_e32 v3, 0x38d1b717, v135
	v_cndmask_b32_e64 v165, v192, v165, s[0:1]
	v_cndmask_b32_e64 v227, v193, v227, s[0:1]
	v_cndmask_b32_e64 v175, v194, v175, s[0:1]
	v_cndmask_b32_e64 v229, v195, v229, s[0:1]
	v_cndmask_b32_e64 v232, v196, v232, s[0:1]
	v_cndmask_b32_e64 v3, v3, v135, s[0:1]
	v_mul_f32_e32 v157, v165, v226
	v_mul_f32_e32 v159, v227, v228
	v_mul_f32_e32 v161, v175, v230
	v_mul_f32_e32 v163, v229, v231
	v_mul_f32_e32 v165, v232, v233
	v_mul_f32_e32 v3, v3, v153
	v_mul_f32_e32 v126, v126, v157
	v_mul_f32_e32 v127, v127, v159
	v_mul_f32_e32 v128, v128, v161
	v_mul_f32_e32 v129, v129, v163
	v_mul_f32_e32 v122, v122, v165
	v_mul_f32_e32 v121, v121, v3
	v_mov_b32_e32 v3, v162
	s_nop 0
	v_mad_i64_i32 v[226:227], s[40:41], v3, s62, v[136:137]
	v_lshl_add_u64 v[234:235], v[226:227], 0, s[16:17]
	v_lshl_add_u64 v[230:231], v[234:235], 0, v[166:167]
	v_lshl_add_u64 v[226:227], v[230:231], 0, s[38:39]
	global_load_dwordx4 v[226:229], v[226:227], off
	v_lshl_add_u64 v[230:231], v[230:231], 0, s[2:3]
	global_load_dwordx4 v[230:233], v[230:231], off
	v_lshl_add_u64 v[238:239], v[234:235], 0, s[2:3]
	v_lshl_add_u64 v[234:235], v[234:235], 0, s[38:39]
	v_lshl_add_u64 v[234:235], v[234:235], 0, v[4:5]
	global_load_dwordx4 v[234:237], v[234:235], off
	v_lshl_add_u64 v[238:239], v[238:239], 0, v[4:5]
	global_load_dwordx4 v[238:241], v[238:239], off
	s_waitcnt vmcnt(4)
	v_cvt_f32_f16_e32 v3, v168
	v_cvt_f32_f16_e32 v135, v176
	v_cvt_f32_f16_sdwa v155, v176 dst_sel:DWORD dst_unused:UNUSED_PAD src0_sel:WORD_1
	v_cvt_f32_f16_e32 v159, v177
	v_cvt_f32_f16_sdwa v153, v168 dst_sel:DWORD dst_unused:UNUSED_PAD src0_sel:WORD_1
	v_max_f32_e32 v135, 0x38d1b717, v135
	v_cvt_f32_f16_e32 v157, v169
	v_rcp_f32_e32 v135, v135
	v_cvt_f32_f16_sdwa v163, v177 dst_sel:DWORD dst_unused:UNUSED_PAD src0_sel:WORD_1
	v_max_f32_e32 v155, 0x38d1b717, v155
	v_max_f32_e32 v159, 0x38d1b717, v159
	v_max_f32_e32 v165, 0x38d1b717, v3
	v_rcp_f32_e32 v155, v155
	v_rcp_f32_e32 v159, v159
	v_cndmask_b32_e64 v3, v165, v3, s[0:1]
	v_cvt_f32_f16_sdwa v161, v169 dst_sel:DWORD dst_unused:UNUSED_PAD src0_sel:WORD_1
	v_max_f32_e32 v168, 0x38d1b717, v153
	v_max_f32_e32 v169, 0x38d1b717, v157
	v_mul_f32_e32 v3, v3, v135
	v_cndmask_b32_e64 v153, v168, v153, s[0:1]
	v_cndmask_b32_e64 v157, v169, v157, s[0:1]
	v_mul_f32_e32 v114, v114, v3
	v_max_f32_e32 v3, 0x38d1b717, v163
	v_mul_f32_e32 v135, v153, v155
	v_mul_f32_e32 v153, v157, v159
	v_rcp_f32_e32 v3, v3
	v_mul_f32_e32 v116, v116, v153
	v_cvt_f32_f16_e32 v153, v178
	v_mul_f32_e32 v115, v115, v135
	v_max_f32_e32 v135, 0x38d1b717, v161
	v_cndmask_b32_e64 v135, v135, v161, s[0:1]
	v_mul_f32_e32 v3, v135, v3
	v_cvt_f32_f16_e32 v135, v170
	v_mul_f32_e32 v117, v117, v3
	v_max_f32_e32 v3, 0x38d1b717, v153
	v_rcp_f32_e32 v3, v3
	v_max_f32_e32 v153, 0x38d1b717, v135
	v_cndmask_b32_e64 v135, v153, v135, s[0:1]
	v_cvt_f32_f16_sdwa v153, v178 dst_sel:DWORD dst_unused:UNUSED_PAD src0_sel:WORD_1
	v_mul_f32_e32 v3, v135, v3
	v_cvt_f32_f16_sdwa v135, v170 dst_sel:DWORD dst_unused:UNUSED_PAD src0_sel:WORD_1
	v_mul_f32_e32 v110, v110, v3
	v_max_f32_e32 v3, 0x38d1b717, v153
	v_rcp_f32_e32 v3, v3
	v_max_f32_e32 v153, 0x38d1b717, v135
	v_cndmask_b32_e64 v135, v153, v135, s[0:1]
	v_cvt_f32_f16_e32 v153, v179
	v_mul_f32_e32 v3, v135, v3
	v_cvt_f32_f16_e32 v135, v171
	v_mul_f32_e32 v111, v111, v3
	v_max_f32_e32 v3, 0x38d1b717, v153
	v_rcp_f32_e32 v3, v3
	v_max_f32_e32 v153, 0x38d1b717, v135
	v_cndmask_b32_e64 v135, v153, v135, s[0:1]
	v_cvt_f32_f16_sdwa v153, v179 dst_sel:DWORD dst_unused:UNUSED_PAD src0_sel:WORD_1
	v_mul_f32_e32 v3, v135, v3
	v_cvt_f32_f16_sdwa v135, v171 dst_sel:DWORD dst_unused:UNUSED_PAD src0_sel:WORD_1
	v_mul_f32_e32 v112, v112, v3
	v_max_f32_e32 v3, 0x38d1b717, v153
	v_rcp_f32_e32 v3, v3
	v_max_f32_e32 v153, 0x38d1b717, v135
	v_cndmask_b32_e64 v135, v153, v135, s[0:1]
	v_cvt_f32_f16_e32 v153, v180
	v_mul_f32_e32 v3, v135, v3
	v_cvt_f32_f16_e32 v135, v184
	v_mul_f32_e32 v113, v113, v3
	v_max_f32_e32 v3, 0x38d1b717, v153
	v_rcp_f32_e32 v3, v3
	v_max_f32_e32 v153, 0x38d1b717, v135
	v_cndmask_b32_e64 v135, v153, v135, s[0:1]
	v_cvt_f32_f16_sdwa v153, v180 dst_sel:DWORD dst_unused:UNUSED_PAD src0_sel:WORD_1
	v_mul_f32_e32 v3, v135, v3
	v_cvt_f32_f16_sdwa v135, v184 dst_sel:DWORD dst_unused:UNUSED_PAD src0_sel:WORD_1
	v_mul_f32_e32 v106, v106, v3
	v_max_f32_e32 v3, 0x38d1b717, v153
	v_rcp_f32_e32 v3, v3
	v_max_f32_e32 v153, 0x38d1b717, v135
	v_cndmask_b32_e64 v135, v153, v135, s[0:1]
	v_cvt_f32_f16_e32 v153, v181
	v_mul_f32_e32 v3, v135, v3
	v_cvt_f32_f16_e32 v135, v185
	v_mul_f32_e32 v107, v107, v3
	v_max_f32_e32 v3, 0x38d1b717, v153
	v_rcp_f32_e32 v3, v3
	v_max_f32_e32 v153, 0x38d1b717, v135
	v_cndmask_b32_e64 v135, v153, v135, s[0:1]
	v_cvt_f32_f16_sdwa v153, v181 dst_sel:DWORD dst_unused:UNUSED_PAD src0_sel:WORD_1
	v_mul_f32_e32 v3, v135, v3
	v_cvt_f32_f16_sdwa v135, v185 dst_sel:DWORD dst_unused:UNUSED_PAD src0_sel:WORD_1
	v_mul_f32_e32 v108, v108, v3
	v_max_f32_e32 v3, 0x38d1b717, v153
	v_rcp_f32_e32 v3, v3
	v_max_f32_e32 v153, 0x38d1b717, v135
	v_cndmask_b32_e64 v135, v153, v135, s[0:1]
	v_cvt_f32_f16_e32 v153, v182
	v_mul_f32_e32 v3, v135, v3
	v_cvt_f32_f16_e32 v135, v186
	v_mul_f32_e32 v109, v109, v3
	v_max_f32_e32 v3, 0x38d1b717, v153
	v_rcp_f32_e32 v3, v3
	v_max_f32_e32 v153, 0x38d1b717, v135
	v_cndmask_b32_e64 v135, v153, v135, s[0:1]
	v_cvt_f32_f16_sdwa v153, v182 dst_sel:DWORD dst_unused:UNUSED_PAD src0_sel:WORD_1
	v_mul_f32_e32 v3, v135, v3
	v_cvt_f32_f16_sdwa v135, v186 dst_sel:DWORD dst_unused:UNUSED_PAD src0_sel:WORD_1
	v_mul_f32_e32 v102, v102, v3
	v_max_f32_e32 v3, 0x38d1b717, v153
	v_rcp_f32_e32 v3, v3
	v_max_f32_e32 v153, 0x38d1b717, v135
	v_cndmask_b32_e64 v135, v153, v135, s[0:1]
	v_cvt_f32_f16_e32 v153, v183
	v_mul_f32_e32 v3, v135, v3
	v_cvt_f32_f16_e32 v135, v187
	v_mul_f32_e32 v103, v103, v3
	v_max_f32_e32 v3, 0x38d1b717, v153
	v_rcp_f32_e32 v3, v3
	v_cvt_f32_f16_sdwa v155, v183 dst_sel:DWORD dst_unused:UNUSED_PAD src0_sel:WORD_1
	v_max_f32_e32 v153, 0x38d1b717, v135
	v_cndmask_b32_e64 v135, v153, v135, s[0:1]
	v_mul_f32_e32 v3, v135, v3
	v_cvt_f32_f16_sdwa v135, v187 dst_sel:DWORD dst_unused:UNUSED_PAD src0_sel:WORD_1
	v_max_f32_e32 v153, 0x38d1b717, v155
	v_rcp_f32_e32 v153, v153
	v_mul_f32_e32 v104, v104, v3
	v_max_f32_e32 v3, 0x38d1b717, v135
	v_cndmask_b32_e64 v3, v3, v135, s[0:1]
	v_mul_f32_e32 v3, v3, v153
	v_mul_f32_e32 v105, v105, v3
	v_mov_b32_e32 v3, v160
	s_nop 0
	v_mad_i64_i32 v[168:169], s[40:41], v3, s62, v[136:137]
	v_lshl_add_u64 v[180:181], v[168:169], 0, s[16:17]
	v_lshl_add_u64 v[176:177], v[180:181], 0, v[166:167]
	v_lshl_add_u64 v[168:169], v[176:177], 0, s[38:39]
	global_load_dwordx4 v[168:171], v[168:169], off
	v_lshl_add_u64 v[176:177], v[176:177], 0, s[2:3]
	global_load_dwordx4 v[176:179], v[176:177], off
	v_lshl_add_u64 v[184:185], v[180:181], 0, s[2:3]
	v_lshl_add_u64 v[180:181], v[180:181], 0, s[38:39]
	v_lshl_add_u64 v[180:181], v[180:181], 0, v[4:5]
	global_load_dwordx4 v[180:183], v[180:181], off
	v_lshl_add_u64 v[184:185], v[184:185], 0, v[4:5]
	global_load_dwordx4 v[184:187], v[184:185], off
	s_waitcnt vmcnt(4)
	v_cvt_f32_f16_e32 v3, v226
	v_cvt_f32_f16_e32 v135, v230
	v_max_f32_e32 v3, 0x38d1b717, v3
	v_rcp_f32_e32 v3, v3
	v_max_f32_e32 v153, 0x38d1b717, v135
	v_cndmask_b32_e64 v135, v153, v135, s[0:1]
	v_cvt_f32_f16_sdwa v153, v226 dst_sel:DWORD dst_unused:UNUSED_PAD src0_sel:WORD_1
	v_mul_f32_e32 v3, v135, v3
	v_cvt_f32_f16_sdwa v135, v230 dst_sel:DWORD dst_unused:UNUSED_PAD src0_sel:WORD_1
	v_mul_f32_e32 v98, v98, v3
	v_max_f32_e32 v3, 0x38d1b717, v153
	v_rcp_f32_e32 v3, v3
	v_max_f32_e32 v153, 0x38d1b717, v135
	v_cndmask_b32_e64 v135, v153, v135, s[0:1]
	v_cvt_f32_f16_e32 v153, v227
	v_mul_f32_e32 v3, v135, v3
	v_cvt_f32_f16_e32 v135, v231
	v_mul_f32_e32 v99, v99, v3
	v_max_f32_e32 v3, 0x38d1b717, v153
	v_rcp_f32_e32 v3, v3
	v_max_f32_e32 v153, 0x38d1b717, v135
	v_cndmask_b32_e64 v135, v153, v135, s[0:1]
	v_cvt_f32_f16_sdwa v153, v227 dst_sel:DWORD dst_unused:UNUSED_PAD src0_sel:WORD_1
	v_mul_f32_e32 v3, v135, v3
	v_cvt_f32_f16_sdwa v135, v231 dst_sel:DWORD dst_unused:UNUSED_PAD src0_sel:WORD_1
	v_mul_f32_e32 v100, v100, v3
	v_max_f32_e32 v3, 0x38d1b717, v153
	v_rcp_f32_e32 v3, v3
	v_max_f32_e32 v153, 0x38d1b717, v135
	v_cndmask_b32_e64 v135, v153, v135, s[0:1]
	v_cvt_f32_f16_e32 v153, v228
	v_mul_f32_e32 v3, v135, v3
	v_cvt_f32_f16_e32 v135, v232
	v_mul_f32_e32 v101, v101, v3
	v_max_f32_e32 v3, 0x38d1b717, v153
	v_rcp_f32_e32 v3, v3
	v_max_f32_e32 v153, 0x38d1b717, v135
	v_cndmask_b32_e64 v135, v153, v135, s[0:1]
	v_cvt_f32_f16_sdwa v153, v228 dst_sel:DWORD dst_unused:UNUSED_PAD src0_sel:WORD_1
	v_mul_f32_e32 v3, v135, v3
	v_cvt_f32_f16_sdwa v135, v232 dst_sel:DWORD dst_unused:UNUSED_PAD src0_sel:WORD_1
	v_mul_f32_e32 v94, v94, v3
	v_max_f32_e32 v3, 0x38d1b717, v153
	v_rcp_f32_e32 v3, v3
	v_max_f32_e32 v153, 0x38d1b717, v135
	v_cndmask_b32_e64 v135, v153, v135, s[0:1]
	v_cvt_f32_f16_e32 v153, v229
	v_mul_f32_e32 v3, v135, v3
	v_cvt_f32_f16_e32 v135, v233
	v_mul_f32_e32 v95, v95, v3
	v_max_f32_e32 v3, 0x38d1b717, v153
	v_rcp_f32_e32 v3, v3
	v_max_f32_e32 v153, 0x38d1b717, v135
	v_cndmask_b32_e64 v135, v153, v135, s[0:1]
	v_cvt_f32_f16_sdwa v153, v229 dst_sel:DWORD dst_unused:UNUSED_PAD src0_sel:WORD_1
	v_mul_f32_e32 v3, v135, v3
	v_cvt_f32_f16_sdwa v135, v233 dst_sel:DWORD dst_unused:UNUSED_PAD src0_sel:WORD_1
	v_mul_f32_e32 v96, v96, v3
	v_max_f32_e32 v3, 0x38d1b717, v153
	v_rcp_f32_e32 v3, v3
	v_max_f32_e32 v153, 0x38d1b717, v135
	v_cndmask_b32_e64 v135, v153, v135, s[0:1]
	v_cvt_f32_f16_e32 v153, v234
	v_mul_f32_e32 v3, v135, v3
	v_cvt_f32_f16_e32 v135, v238
	v_mul_f32_e32 v97, v97, v3
	v_max_f32_e32 v3, 0x38d1b717, v153
	v_rcp_f32_e32 v3, v3
	v_max_f32_e32 v153, 0x38d1b717, v135
	v_cndmask_b32_e64 v135, v153, v135, s[0:1]
	v_cvt_f32_f16_sdwa v153, v234 dst_sel:DWORD dst_unused:UNUSED_PAD src0_sel:WORD_1
	v_mul_f32_e32 v3, v135, v3
	v_cvt_f32_f16_sdwa v135, v238 dst_sel:DWORD dst_unused:UNUSED_PAD src0_sel:WORD_1
	v_mul_f32_e32 v90, v90, v3
	v_max_f32_e32 v3, 0x38d1b717, v153
	v_rcp_f32_e32 v3, v3
	v_max_f32_e32 v153, 0x38d1b717, v135
	v_cndmask_b32_e64 v135, v153, v135, s[0:1]
	v_cvt_f32_f16_e32 v153, v235
	v_mul_f32_e32 v3, v135, v3
	v_cvt_f32_f16_e32 v135, v239
	v_mul_f32_e32 v91, v91, v3
	v_max_f32_e32 v3, 0x38d1b717, v153
	v_rcp_f32_e32 v3, v3
	v_max_f32_e32 v153, 0x38d1b717, v135
	v_cndmask_b32_e64 v135, v153, v135, s[0:1]
	v_cvt_f32_f16_sdwa v153, v235 dst_sel:DWORD dst_unused:UNUSED_PAD src0_sel:WORD_1
	v_mul_f32_e32 v3, v135, v3
	v_cvt_f32_f16_sdwa v135, v239 dst_sel:DWORD dst_unused:UNUSED_PAD src0_sel:WORD_1
	v_mul_f32_e32 v92, v92, v3
	v_max_f32_e32 v3, 0x38d1b717, v153
	v_rcp_f32_e32 v3, v3
	v_max_f32_e32 v153, 0x38d1b717, v135
	v_cndmask_b32_e64 v135, v153, v135, s[0:1]
	v_cvt_f32_f16_e32 v153, v236
	v_mul_f32_e32 v3, v135, v3
	v_cvt_f32_f16_e32 v135, v240
	v_mul_f32_e32 v93, v93, v3
	v_max_f32_e32 v3, 0x38d1b717, v153
	v_rcp_f32_e32 v3, v3
	v_max_f32_e32 v153, 0x38d1b717, v135
	v_cndmask_b32_e64 v135, v153, v135, s[0:1]
	v_cvt_f32_f16_sdwa v153, v236 dst_sel:DWORD dst_unused:UNUSED_PAD src0_sel:WORD_1
	v_mul_f32_e32 v3, v135, v3
	v_cvt_f32_f16_sdwa v135, v240 dst_sel:DWORD dst_unused:UNUSED_PAD src0_sel:WORD_1
	v_mul_f32_e32 v86, v86, v3
	v_max_f32_e32 v3, 0x38d1b717, v153
	v_rcp_f32_e32 v3, v3
	v_max_f32_e32 v153, 0x38d1b717, v135
	v_cndmask_b32_e64 v135, v153, v135, s[0:1]
	v_cvt_f32_f16_e32 v153, v237
	v_mul_f32_e32 v3, v135, v3
	v_cvt_f32_f16_e32 v135, v241
	v_mul_f32_e32 v87, v87, v3
	v_max_f32_e32 v3, 0x38d1b717, v153
	v_rcp_f32_e32 v3, v3
	v_cvt_f32_f16_sdwa v155, v237 dst_sel:DWORD dst_unused:UNUSED_PAD src0_sel:WORD_1
	v_max_f32_e32 v153, 0x38d1b717, v135
	v_cndmask_b32_e64 v135, v153, v135, s[0:1]
	v_mul_f32_e32 v3, v135, v3
	v_cvt_f32_f16_sdwa v135, v241 dst_sel:DWORD dst_unused:UNUSED_PAD src0_sel:WORD_1
	v_max_f32_e32 v153, 0x38d1b717, v155
	v_rcp_f32_e32 v153, v153
	v_mul_f32_e32 v88, v88, v3
	v_max_f32_e32 v3, 0x38d1b717, v135
	v_cndmask_b32_e64 v3, v3, v135, s[0:1]
	v_mul_f32_e32 v3, v3, v153
	v_mul_f32_e32 v89, v89, v3
	v_mov_b32_e32 v3, v158
	s_nop 0
	v_mad_i64_i32 v[226:227], s[40:41], v3, s62, v[136:137]
	v_lshl_add_u64 v[234:235], v[226:227], 0, s[16:17]
	v_lshl_add_u64 v[230:231], v[234:235], 0, v[166:167]
	v_lshl_add_u64 v[226:227], v[230:231], 0, s[38:39]
	global_load_dwordx4 v[226:229], v[226:227], off
	v_lshl_add_u64 v[230:231], v[230:231], 0, s[2:3]
	global_load_dwordx4 v[230:233], v[230:231], off
	v_lshl_add_u64 v[238:239], v[234:235], 0, s[2:3]
	v_lshl_add_u64 v[234:235], v[234:235], 0, s[38:39]
	v_lshl_add_u64 v[234:235], v[234:235], 0, v[4:5]
	global_load_dwordx4 v[234:237], v[234:235], off
	v_lshl_add_u64 v[238:239], v[238:239], 0, v[4:5]
	global_load_dwordx4 v[238:241], v[238:239], off
	s_waitcnt vmcnt(4)
	v_cvt_f32_f16_e32 v3, v168
	v_cvt_f32_f16_e32 v135, v176
	v_max_f32_e32 v3, 0x38d1b717, v3
	v_rcp_f32_e32 v3, v3
	v_max_f32_e32 v153, 0x38d1b717, v135
	v_cndmask_b32_e64 v135, v153, v135, s[0:1]
	v_cvt_f32_f16_sdwa v153, v168 dst_sel:DWORD dst_unused:UNUSED_PAD src0_sel:WORD_1
	v_mul_f32_e32 v3, v135, v3
	v_cvt_f32_f16_sdwa v135, v176 dst_sel:DWORD dst_unused:UNUSED_PAD src0_sel:WORD_1
	v_mul_f32_e32 v82, v82, v3
	v_max_f32_e32 v3, 0x38d1b717, v153
	v_rcp_f32_e32 v3, v3
	v_max_f32_e32 v153, 0x38d1b717, v135
	v_cndmask_b32_e64 v135, v153, v135, s[0:1]
	v_cvt_f32_f16_e32 v153, v169
	v_mul_f32_e32 v3, v135, v3
	v_cvt_f32_f16_e32 v135, v177
	v_mul_f32_e32 v83, v83, v3
	v_max_f32_e32 v3, 0x38d1b717, v153
	v_rcp_f32_e32 v3, v3
	v_max_f32_e32 v153, 0x38d1b717, v135
	v_cndmask_b32_e64 v135, v153, v135, s[0:1]
	v_cvt_f32_f16_sdwa v153, v169 dst_sel:DWORD dst_unused:UNUSED_PAD src0_sel:WORD_1
	v_mul_f32_e32 v3, v135, v3
	v_cvt_f32_f16_sdwa v135, v177 dst_sel:DWORD dst_unused:UNUSED_PAD src0_sel:WORD_1
	v_mul_f32_e32 v84, v84, v3
	v_max_f32_e32 v3, 0x38d1b717, v153
	v_rcp_f32_e32 v3, v3
	v_max_f32_e32 v153, 0x38d1b717, v135
	v_cndmask_b32_e64 v135, v153, v135, s[0:1]
	v_cvt_f32_f16_e32 v153, v170
	v_mul_f32_e32 v3, v135, v3
	v_cvt_f32_f16_e32 v135, v178
	v_mul_f32_e32 v85, v85, v3
	v_max_f32_e32 v3, 0x38d1b717, v153
	v_rcp_f32_e32 v3, v3
	v_max_f32_e32 v153, 0x38d1b717, v135
	v_cndmask_b32_e64 v135, v153, v135, s[0:1]
	v_cvt_f32_f16_sdwa v153, v170 dst_sel:DWORD dst_unused:UNUSED_PAD src0_sel:WORD_1
	v_mul_f32_e32 v3, v135, v3
	v_cvt_f32_f16_sdwa v135, v178 dst_sel:DWORD dst_unused:UNUSED_PAD src0_sel:WORD_1
	v_mul_f32_e32 v78, v78, v3
	v_max_f32_e32 v3, 0x38d1b717, v153
	v_rcp_f32_e32 v3, v3
	v_max_f32_e32 v153, 0x38d1b717, v135
	v_cndmask_b32_e64 v135, v153, v135, s[0:1]
	v_cvt_f32_f16_e32 v153, v171
	v_mul_f32_e32 v3, v135, v3
	v_cvt_f32_f16_e32 v135, v179
	v_mul_f32_e32 v79, v79, v3
	v_max_f32_e32 v3, 0x38d1b717, v153
	v_rcp_f32_e32 v3, v3
	v_max_f32_e32 v153, 0x38d1b717, v135
	v_cndmask_b32_e64 v135, v153, v135, s[0:1]
	v_cvt_f32_f16_sdwa v153, v171 dst_sel:DWORD dst_unused:UNUSED_PAD src0_sel:WORD_1
	v_mul_f32_e32 v3, v135, v3
	v_cvt_f32_f16_sdwa v135, v179 dst_sel:DWORD dst_unused:UNUSED_PAD src0_sel:WORD_1
	v_mul_f32_e32 v80, v80, v3
	v_max_f32_e32 v3, 0x38d1b717, v153
	v_rcp_f32_e32 v3, v3
	v_max_f32_e32 v153, 0x38d1b717, v135
	v_cndmask_b32_e64 v135, v153, v135, s[0:1]
	v_cvt_f32_f16_e32 v153, v180
	v_mul_f32_e32 v3, v135, v3
	v_cvt_f32_f16_e32 v135, v184
	v_mul_f32_e32 v81, v81, v3
	v_max_f32_e32 v3, 0x38d1b717, v153
	v_rcp_f32_e32 v3, v3
	v_max_f32_e32 v153, 0x38d1b717, v135
	v_cndmask_b32_e64 v135, v153, v135, s[0:1]
	v_cvt_f32_f16_sdwa v153, v180 dst_sel:DWORD dst_unused:UNUSED_PAD src0_sel:WORD_1
	v_mul_f32_e32 v3, v135, v3
	v_cvt_f32_f16_sdwa v135, v184 dst_sel:DWORD dst_unused:UNUSED_PAD src0_sel:WORD_1
	v_mul_f32_e32 v74, v74, v3
	v_max_f32_e32 v3, 0x38d1b717, v153
	v_rcp_f32_e32 v3, v3
	v_max_f32_e32 v153, 0x38d1b717, v135
	v_cndmask_b32_e64 v135, v153, v135, s[0:1]
	v_cvt_f32_f16_e32 v153, v181
	v_mul_f32_e32 v3, v135, v3
	v_cvt_f32_f16_e32 v135, v185
	v_mul_f32_e32 v75, v75, v3
	v_max_f32_e32 v3, 0x38d1b717, v153
	v_rcp_f32_e32 v3, v3
	v_max_f32_e32 v153, 0x38d1b717, v135
	v_cndmask_b32_e64 v135, v153, v135, s[0:1]
	v_cvt_f32_f16_sdwa v153, v181 dst_sel:DWORD dst_unused:UNUSED_PAD src0_sel:WORD_1
	v_mul_f32_e32 v3, v135, v3
	v_cvt_f32_f16_sdwa v135, v185 dst_sel:DWORD dst_unused:UNUSED_PAD src0_sel:WORD_1
	v_mul_f32_e32 v76, v76, v3
	v_max_f32_e32 v3, 0x38d1b717, v153
	v_rcp_f32_e32 v3, v3
	v_max_f32_e32 v153, 0x38d1b717, v135
	v_cndmask_b32_e64 v135, v153, v135, s[0:1]
	v_cvt_f32_f16_e32 v153, v182
	v_mul_f32_e32 v3, v135, v3
	v_cvt_f32_f16_e32 v135, v186
	v_mul_f32_e32 v77, v77, v3
	v_max_f32_e32 v3, 0x38d1b717, v153
	v_rcp_f32_e32 v3, v3
	v_max_f32_e32 v153, 0x38d1b717, v135
	v_cndmask_b32_e64 v135, v153, v135, s[0:1]
	v_cvt_f32_f16_sdwa v153, v182 dst_sel:DWORD dst_unused:UNUSED_PAD src0_sel:WORD_1
	v_mul_f32_e32 v3, v135, v3
	v_cvt_f32_f16_sdwa v135, v186 dst_sel:DWORD dst_unused:UNUSED_PAD src0_sel:WORD_1
	v_mul_f32_e32 v70, v70, v3
	v_max_f32_e32 v3, 0x38d1b717, v153
	v_rcp_f32_e32 v3, v3
	v_max_f32_e32 v153, 0x38d1b717, v135
	v_cndmask_b32_e64 v135, v153, v135, s[0:1]
	v_cvt_f32_f16_e32 v153, v183
	v_mul_f32_e32 v3, v135, v3
	v_cvt_f32_f16_e32 v135, v187
	v_mul_f32_e32 v71, v71, v3
	v_max_f32_e32 v3, 0x38d1b717, v153
	v_rcp_f32_e32 v3, v3
	v_cvt_f32_f16_sdwa v155, v183 dst_sel:DWORD dst_unused:UNUSED_PAD src0_sel:WORD_1
	v_max_f32_e32 v153, 0x38d1b717, v135
	v_cndmask_b32_e64 v135, v153, v135, s[0:1]
	v_mul_f32_e32 v3, v135, v3
	v_cvt_f32_f16_sdwa v135, v187 dst_sel:DWORD dst_unused:UNUSED_PAD src0_sel:WORD_1
	v_max_f32_e32 v153, 0x38d1b717, v155
	v_rcp_f32_e32 v153, v153
	v_mul_f32_e32 v72, v72, v3
	v_max_f32_e32 v3, 0x38d1b717, v135
	v_cndmask_b32_e64 v3, v3, v135, s[0:1]
	v_mul_f32_e32 v3, v3, v153
	v_mul_f32_e32 v73, v73, v3
	v_mov_b32_e32 v3, v156
	s_nop 0
	v_mad_i64_i32 v[168:169], s[40:41], v3, s62, v[136:137]
	v_lshl_add_u64 v[180:181], v[168:169], 0, s[16:17]
	v_lshl_add_u64 v[176:177], v[180:181], 0, v[166:167]
	v_lshl_add_u64 v[168:169], v[176:177], 0, s[38:39]
	global_load_dwordx4 v[168:171], v[168:169], off
	v_lshl_add_u64 v[176:177], v[176:177], 0, s[2:3]
	global_load_dwordx4 v[176:179], v[176:177], off
	v_lshl_add_u64 v[184:185], v[180:181], 0, s[2:3]
	v_lshl_add_u64 v[180:181], v[180:181], 0, s[38:39]
	v_lshl_add_u64 v[180:181], v[180:181], 0, v[4:5]
	global_load_dwordx4 v[180:183], v[180:181], off
	v_lshl_add_u64 v[184:185], v[184:185], 0, v[4:5]
	global_load_dwordx4 v[184:187], v[184:185], off
	s_waitcnt vmcnt(4)
	v_cvt_f32_f16_e32 v3, v226
	v_cvt_f32_f16_e32 v135, v230
	v_max_f32_e32 v3, 0x38d1b717, v3
	v_rcp_f32_e32 v3, v3
	v_max_f32_e32 v153, 0x38d1b717, v135
	v_cndmask_b32_e64 v135, v153, v135, s[0:1]
	v_cvt_f32_f16_sdwa v153, v226 dst_sel:DWORD dst_unused:UNUSED_PAD src0_sel:WORD_1
	v_mul_f32_e32 v3, v135, v3
	v_cvt_f32_f16_sdwa v135, v230 dst_sel:DWORD dst_unused:UNUSED_PAD src0_sel:WORD_1
	v_mul_f32_e32 v66, v66, v3
	v_max_f32_e32 v3, 0x38d1b717, v153
	v_rcp_f32_e32 v3, v3
	v_max_f32_e32 v153, 0x38d1b717, v135
	v_cndmask_b32_e64 v135, v153, v135, s[0:1]
	v_cvt_f32_f16_e32 v153, v227
	v_mul_f32_e32 v3, v135, v3
	v_cvt_f32_f16_e32 v135, v231
	v_mul_f32_e32 v67, v67, v3
	v_max_f32_e32 v3, 0x38d1b717, v153
	v_rcp_f32_e32 v3, v3
	v_max_f32_e32 v153, 0x38d1b717, v135
	v_cndmask_b32_e64 v135, v153, v135, s[0:1]
	v_cvt_f32_f16_sdwa v153, v227 dst_sel:DWORD dst_unused:UNUSED_PAD src0_sel:WORD_1
	v_mul_f32_e32 v3, v135, v3
	v_cvt_f32_f16_sdwa v135, v231 dst_sel:DWORD dst_unused:UNUSED_PAD src0_sel:WORD_1
	v_mul_f32_e32 v68, v68, v3
	v_max_f32_e32 v3, 0x38d1b717, v153
	v_rcp_f32_e32 v3, v3
	v_max_f32_e32 v153, 0x38d1b717, v135
	v_cndmask_b32_e64 v135, v153, v135, s[0:1]
	v_cvt_f32_f16_e32 v153, v228
	v_mul_f32_e32 v3, v135, v3
	v_cvt_f32_f16_e32 v135, v232
	v_mul_f32_e32 v69, v69, v3
	v_max_f32_e32 v3, 0x38d1b717, v153
	v_rcp_f32_e32 v3, v3
	v_max_f32_e32 v153, 0x38d1b717, v135
	v_cndmask_b32_e64 v135, v153, v135, s[0:1]
	v_cvt_f32_f16_sdwa v153, v228 dst_sel:DWORD dst_unused:UNUSED_PAD src0_sel:WORD_1
	v_mul_f32_e32 v3, v135, v3
	v_cvt_f32_f16_sdwa v135, v232 dst_sel:DWORD dst_unused:UNUSED_PAD src0_sel:WORD_1
	v_mul_f32_e32 v62, v62, v3
	v_max_f32_e32 v3, 0x38d1b717, v153
	v_rcp_f32_e32 v3, v3
	v_max_f32_e32 v153, 0x38d1b717, v135
	v_cndmask_b32_e64 v135, v153, v135, s[0:1]
	v_cvt_f32_f16_e32 v153, v229
	v_mul_f32_e32 v3, v135, v3
	v_cvt_f32_f16_e32 v135, v233
	v_mul_f32_e32 v63, v63, v3
	v_max_f32_e32 v3, 0x38d1b717, v153
	v_rcp_f32_e32 v3, v3
	v_max_f32_e32 v153, 0x38d1b717, v135
	v_cndmask_b32_e64 v135, v153, v135, s[0:1]
	v_cvt_f32_f16_sdwa v153, v229 dst_sel:DWORD dst_unused:UNUSED_PAD src0_sel:WORD_1
	v_mul_f32_e32 v3, v135, v3
	v_cvt_f32_f16_sdwa v135, v233 dst_sel:DWORD dst_unused:UNUSED_PAD src0_sel:WORD_1
	v_mul_f32_e32 v64, v64, v3
	v_max_f32_e32 v3, 0x38d1b717, v153
	v_rcp_f32_e32 v3, v3
	v_max_f32_e32 v153, 0x38d1b717, v135
	v_cndmask_b32_e64 v135, v153, v135, s[0:1]
	v_cvt_f32_f16_e32 v153, v234
	v_mul_f32_e32 v3, v135, v3
	v_cvt_f32_f16_e32 v135, v238
	v_mul_f32_e32 v65, v65, v3
	v_max_f32_e32 v3, 0x38d1b717, v153
	v_rcp_f32_e32 v3, v3
	v_max_f32_e32 v153, 0x38d1b717, v135
	v_cndmask_b32_e64 v135, v153, v135, s[0:1]
	v_cvt_f32_f16_sdwa v153, v234 dst_sel:DWORD dst_unused:UNUSED_PAD src0_sel:WORD_1
	v_mul_f32_e32 v3, v135, v3
	v_cvt_f32_f16_sdwa v135, v238 dst_sel:DWORD dst_unused:UNUSED_PAD src0_sel:WORD_1
	v_mul_f32_e32 v58, v58, v3
	v_max_f32_e32 v3, 0x38d1b717, v153
	v_rcp_f32_e32 v3, v3
	v_max_f32_e32 v153, 0x38d1b717, v135
	v_cndmask_b32_e64 v135, v153, v135, s[0:1]
	v_cvt_f32_f16_e32 v153, v235
	v_mul_f32_e32 v3, v135, v3
	v_cvt_f32_f16_e32 v135, v239
	v_mul_f32_e32 v59, v59, v3
	v_max_f32_e32 v3, 0x38d1b717, v153
	v_rcp_f32_e32 v3, v3
	v_max_f32_e32 v153, 0x38d1b717, v135
	v_cndmask_b32_e64 v135, v153, v135, s[0:1]
	v_cvt_f32_f16_sdwa v153, v235 dst_sel:DWORD dst_unused:UNUSED_PAD src0_sel:WORD_1
	v_mul_f32_e32 v3, v135, v3
	v_cvt_f32_f16_sdwa v135, v239 dst_sel:DWORD dst_unused:UNUSED_PAD src0_sel:WORD_1
	v_mul_f32_e32 v60, v60, v3
	v_max_f32_e32 v3, 0x38d1b717, v153
	v_rcp_f32_e32 v3, v3
	v_max_f32_e32 v153, 0x38d1b717, v135
	v_cndmask_b32_e64 v135, v153, v135, s[0:1]
	v_cvt_f32_f16_e32 v153, v236
	v_mul_f32_e32 v3, v135, v3
	v_cvt_f32_f16_e32 v135, v240
	v_mul_f32_e32 v61, v61, v3
	v_max_f32_e32 v3, 0x38d1b717, v153
	v_rcp_f32_e32 v3, v3
	v_max_f32_e32 v153, 0x38d1b717, v135
	v_cndmask_b32_e64 v135, v153, v135, s[0:1]
	v_cvt_f32_f16_sdwa v153, v236 dst_sel:DWORD dst_unused:UNUSED_PAD src0_sel:WORD_1
	v_mul_f32_e32 v3, v135, v3
	v_cvt_f32_f16_sdwa v135, v240 dst_sel:DWORD dst_unused:UNUSED_PAD src0_sel:WORD_1
	v_mul_f32_e32 v54, v54, v3
	v_max_f32_e32 v3, 0x38d1b717, v153
	v_rcp_f32_e32 v3, v3
	v_max_f32_e32 v153, 0x38d1b717, v135
	v_cndmask_b32_e64 v135, v153, v135, s[0:1]
	v_cvt_f32_f16_e32 v153, v237
	v_mul_f32_e32 v3, v135, v3
	v_cvt_f32_f16_e32 v135, v241
	v_mul_f32_e32 v55, v55, v3
	v_max_f32_e32 v3, 0x38d1b717, v153
	v_rcp_f32_e32 v3, v3
	v_cvt_f32_f16_sdwa v155, v237 dst_sel:DWORD dst_unused:UNUSED_PAD src0_sel:WORD_1
	v_max_f32_e32 v153, 0x38d1b717, v135
	v_cndmask_b32_e64 v135, v153, v135, s[0:1]
	v_mul_f32_e32 v3, v135, v3
	v_cvt_f32_f16_sdwa v135, v241 dst_sel:DWORD dst_unused:UNUSED_PAD src0_sel:WORD_1
	v_max_f32_e32 v153, 0x38d1b717, v155
	v_rcp_f32_e32 v153, v153
	v_mul_f32_e32 v56, v56, v3
	v_max_f32_e32 v3, 0x38d1b717, v135
	v_cndmask_b32_e64 v3, v3, v135, s[0:1]
	v_mul_f32_e32 v3, v3, v153
	v_mul_f32_e32 v57, v57, v3
	v_mov_b32_e32 v3, v154
	s_nop 0
	v_mad_i64_i32 v[226:227], s[40:41], v3, s62, v[136:137]
	v_lshl_add_u64 v[234:235], v[226:227], 0, s[16:17]
	v_lshl_add_u64 v[230:231], v[234:235], 0, v[166:167]
	v_lshl_add_u64 v[226:227], v[230:231], 0, s[38:39]
	global_load_dwordx4 v[226:229], v[226:227], off
	v_lshl_add_u64 v[230:231], v[230:231], 0, s[2:3]
	global_load_dwordx4 v[230:233], v[230:231], off
	v_lshl_add_u64 v[238:239], v[234:235], 0, s[2:3]
	v_lshl_add_u64 v[234:235], v[234:235], 0, s[38:39]
	v_lshl_add_u64 v[234:235], v[234:235], 0, v[4:5]
	global_load_dwordx4 v[234:237], v[234:235], off
	v_lshl_add_u64 v[238:239], v[238:239], 0, v[4:5]
	global_load_dwordx4 v[238:241], v[238:239], off
	s_waitcnt vmcnt(4)
	v_cvt_f32_f16_e32 v3, v168
	v_cvt_f32_f16_e32 v135, v176
	v_max_f32_e32 v3, 0x38d1b717, v3
	v_rcp_f32_e32 v3, v3
	v_max_f32_e32 v153, 0x38d1b717, v135
	v_cndmask_b32_e64 v135, v153, v135, s[0:1]
	v_cvt_f32_f16_sdwa v153, v168 dst_sel:DWORD dst_unused:UNUSED_PAD src0_sel:WORD_1
	v_mul_f32_e32 v3, v135, v3
	v_cvt_f32_f16_sdwa v135, v176 dst_sel:DWORD dst_unused:UNUSED_PAD src0_sel:WORD_1
	v_mul_f32_e32 v50, v50, v3
	v_max_f32_e32 v3, 0x38d1b717, v153
	v_rcp_f32_e32 v3, v3
	v_max_f32_e32 v153, 0x38d1b717, v135
	v_cndmask_b32_e64 v135, v153, v135, s[0:1]
	v_cvt_f32_f16_e32 v153, v169
	v_mul_f32_e32 v3, v135, v3
	v_cvt_f32_f16_e32 v135, v177
	v_mul_f32_e32 v51, v51, v3
	v_max_f32_e32 v3, 0x38d1b717, v153
	v_rcp_f32_e32 v3, v3
	v_max_f32_e32 v153, 0x38d1b717, v135
	v_cndmask_b32_e64 v135, v153, v135, s[0:1]
	v_cvt_f32_f16_sdwa v153, v169 dst_sel:DWORD dst_unused:UNUSED_PAD src0_sel:WORD_1
	v_mul_f32_e32 v3, v135, v3
	v_cvt_f32_f16_sdwa v135, v177 dst_sel:DWORD dst_unused:UNUSED_PAD src0_sel:WORD_1
	v_mul_f32_e32 v52, v52, v3
	v_max_f32_e32 v3, 0x38d1b717, v153
	v_rcp_f32_e32 v3, v3
	v_max_f32_e32 v153, 0x38d1b717, v135
	v_cndmask_b32_e64 v135, v153, v135, s[0:1]
	v_cvt_f32_f16_e32 v153, v170
	v_mul_f32_e32 v3, v135, v3
	v_cvt_f32_f16_e32 v135, v178
	v_mul_f32_e32 v53, v53, v3
	v_max_f32_e32 v3, 0x38d1b717, v153
	v_rcp_f32_e32 v3, v3
	v_max_f32_e32 v153, 0x38d1b717, v135
	v_cndmask_b32_e64 v135, v153, v135, s[0:1]
	v_cvt_f32_f16_sdwa v153, v170 dst_sel:DWORD dst_unused:UNUSED_PAD src0_sel:WORD_1
	v_mul_f32_e32 v3, v135, v3
	v_cvt_f32_f16_sdwa v135, v178 dst_sel:DWORD dst_unused:UNUSED_PAD src0_sel:WORD_1
	v_mul_f32_e32 v46, v46, v3
	v_max_f32_e32 v3, 0x38d1b717, v153
	v_rcp_f32_e32 v3, v3
	v_max_f32_e32 v153, 0x38d1b717, v135
	v_cndmask_b32_e64 v135, v153, v135, s[0:1]
	v_cvt_f32_f16_e32 v153, v171
	v_mul_f32_e32 v3, v135, v3
	v_cvt_f32_f16_e32 v135, v179
	v_mul_f32_e32 v47, v47, v3
	v_max_f32_e32 v3, 0x38d1b717, v153
	v_rcp_f32_e32 v3, v3
	v_max_f32_e32 v153, 0x38d1b717, v135
	v_cndmask_b32_e64 v135, v153, v135, s[0:1]
	v_cvt_f32_f16_sdwa v153, v171 dst_sel:DWORD dst_unused:UNUSED_PAD src0_sel:WORD_1
	v_mul_f32_e32 v3, v135, v3
	v_cvt_f32_f16_sdwa v135, v179 dst_sel:DWORD dst_unused:UNUSED_PAD src0_sel:WORD_1
	v_mul_f32_e32 v48, v48, v3
	v_max_f32_e32 v3, 0x38d1b717, v153
	v_rcp_f32_e32 v3, v3
	v_max_f32_e32 v153, 0x38d1b717, v135
	v_cndmask_b32_e64 v135, v153, v135, s[0:1]
	v_cvt_f32_f16_e32 v153, v180
	v_mul_f32_e32 v3, v135, v3
	v_cvt_f32_f16_e32 v135, v184
	v_mul_f32_e32 v49, v49, v3
	v_max_f32_e32 v3, 0x38d1b717, v153
	v_rcp_f32_e32 v3, v3
	v_max_f32_e32 v153, 0x38d1b717, v135
	v_cndmask_b32_e64 v135, v153, v135, s[0:1]
	v_cvt_f32_f16_sdwa v153, v180 dst_sel:DWORD dst_unused:UNUSED_PAD src0_sel:WORD_1
	v_mul_f32_e32 v3, v135, v3
	v_cvt_f32_f16_sdwa v135, v184 dst_sel:DWORD dst_unused:UNUSED_PAD src0_sel:WORD_1
	v_mul_f32_e32 v42, v42, v3
	v_max_f32_e32 v3, 0x38d1b717, v153
	v_rcp_f32_e32 v3, v3
	v_max_f32_e32 v153, 0x38d1b717, v135
	v_cndmask_b32_e64 v135, v153, v135, s[0:1]
	v_cvt_f32_f16_e32 v153, v181
	v_mul_f32_e32 v3, v135, v3
	v_cvt_f32_f16_e32 v135, v185
	v_mul_f32_e32 v43, v43, v3
	v_max_f32_e32 v3, 0x38d1b717, v153
	v_rcp_f32_e32 v3, v3
	v_max_f32_e32 v153, 0x38d1b717, v135
	v_cndmask_b32_e64 v135, v153, v135, s[0:1]
	v_cvt_f32_f16_sdwa v153, v181 dst_sel:DWORD dst_unused:UNUSED_PAD src0_sel:WORD_1
	v_mul_f32_e32 v3, v135, v3
	v_cvt_f32_f16_sdwa v135, v185 dst_sel:DWORD dst_unused:UNUSED_PAD src0_sel:WORD_1
	v_mul_f32_e32 v44, v44, v3
	v_max_f32_e32 v3, 0x38d1b717, v153
	v_rcp_f32_e32 v3, v3
	v_max_f32_e32 v153, 0x38d1b717, v135
	v_cndmask_b32_e64 v135, v153, v135, s[0:1]
	v_cvt_f32_f16_e32 v153, v182
	v_mul_f32_e32 v3, v135, v3
	v_cvt_f32_f16_e32 v135, v186
	v_mul_f32_e32 v45, v45, v3
	v_max_f32_e32 v3, 0x38d1b717, v153
	v_rcp_f32_e32 v3, v3
	v_max_f32_e32 v153, 0x38d1b717, v135
	v_cndmask_b32_e64 v135, v153, v135, s[0:1]
	v_cvt_f32_f16_sdwa v153, v182 dst_sel:DWORD dst_unused:UNUSED_PAD src0_sel:WORD_1
	v_mul_f32_e32 v3, v135, v3
	v_cvt_f32_f16_sdwa v135, v186 dst_sel:DWORD dst_unused:UNUSED_PAD src0_sel:WORD_1
	v_mul_f32_e32 v38, v38, v3
	v_max_f32_e32 v3, 0x38d1b717, v153
	v_rcp_f32_e32 v3, v3
	v_max_f32_e32 v153, 0x38d1b717, v135
	v_cndmask_b32_e64 v135, v153, v135, s[0:1]
	v_cvt_f32_f16_e32 v153, v183
	v_mul_f32_e32 v3, v135, v3
	v_cvt_f32_f16_e32 v135, v187
	v_mul_f32_e32 v39, v39, v3
	v_max_f32_e32 v3, 0x38d1b717, v153
	v_rcp_f32_e32 v3, v3
	v_cvt_f32_f16_sdwa v155, v183 dst_sel:DWORD dst_unused:UNUSED_PAD src0_sel:WORD_1
	v_max_f32_e32 v153, 0x38d1b717, v135
	v_cndmask_b32_e64 v135, v153, v135, s[0:1]
	v_mul_f32_e32 v3, v135, v3
	v_cvt_f32_f16_sdwa v135, v187 dst_sel:DWORD dst_unused:UNUSED_PAD src0_sel:WORD_1
	v_max_f32_e32 v153, 0x38d1b717, v155
	v_rcp_f32_e32 v153, v153
	v_mul_f32_e32 v40, v40, v3
	v_max_f32_e32 v3, 0x38d1b717, v135
	v_cndmask_b32_e64 v3, v3, v135, s[0:1]
	v_mul_f32_e32 v3, v3, v153
	v_mul_f32_e32 v41, v41, v3
	v_mov_b32_e32 v3, v152
	s_nop 0
	v_mad_i64_i32 v[136:137], s[40:41], v3, s62, v[136:137]
	v_lshl_add_u64 v[136:137], v[136:137], 0, s[16:17]
	v_lshl_add_u64 v[170:171], v[136:137], 0, v[166:167]
	v_lshl_add_u64 v[166:167], v[170:171], 0, s[38:39]
	global_load_dwordx4 v[166:169], v[166:167], off
	v_lshl_add_u64 v[170:171], v[170:171], 0, s[2:3]
	global_load_dwordx4 v[176:179], v[170:171], off
	v_lshl_add_u64 v[170:171], v[136:137], 0, s[2:3]
	v_lshl_add_u64 v[136:137], v[136:137], 0, s[38:39]
	v_lshl_add_u64 v[136:137], v[136:137], 0, v[4:5]
	global_load_dwordx4 v[180:183], v[136:137], off
	v_lshl_add_u64 v[4:5], v[170:171], 0, v[4:5]
	global_load_dwordx4 v[184:187], v[4:5], off
	s_waitcnt vmcnt(4)
	v_cvt_f32_f16_e32 v3, v226
	v_cvt_f32_f16_e32 v135, v230
	v_max_f32_e32 v3, 0x38d1b717, v3
	v_rcp_f32_e32 v3, v3
	v_max_f32_e32 v153, 0x38d1b717, v135
	v_cndmask_b32_e64 v135, v153, v135, s[0:1]
	v_cvt_f32_f16_sdwa v153, v226 dst_sel:DWORD dst_unused:UNUSED_PAD src0_sel:WORD_1
	v_mul_f32_e32 v3, v135, v3
	v_cvt_f32_f16_sdwa v135, v230 dst_sel:DWORD dst_unused:UNUSED_PAD src0_sel:WORD_1
	v_mul_f32_e32 v34, v34, v3
	v_max_f32_e32 v3, 0x38d1b717, v153
	v_rcp_f32_e32 v3, v3
	v_max_f32_e32 v153, 0x38d1b717, v135
	v_cndmask_b32_e64 v135, v153, v135, s[0:1]
	v_cvt_f32_f16_e32 v153, v227
	v_mul_f32_e32 v3, v135, v3
	v_cvt_f32_f16_e32 v135, v231
	v_mul_f32_e32 v35, v35, v3
	v_max_f32_e32 v3, 0x38d1b717, v153
	v_rcp_f32_e32 v3, v3
	v_max_f32_e32 v153, 0x38d1b717, v135
	v_cndmask_b32_e64 v135, v153, v135, s[0:1]
	v_cvt_f32_f16_sdwa v153, v227 dst_sel:DWORD dst_unused:UNUSED_PAD src0_sel:WORD_1
	v_mul_f32_e32 v3, v135, v3
	v_cvt_f32_f16_sdwa v135, v231 dst_sel:DWORD dst_unused:UNUSED_PAD src0_sel:WORD_1
	v_mul_f32_e32 v36, v36, v3
	v_max_f32_e32 v3, 0x38d1b717, v153
	v_rcp_f32_e32 v3, v3
	v_max_f32_e32 v153, 0x38d1b717, v135
	v_cndmask_b32_e64 v135, v153, v135, s[0:1]
	v_cvt_f32_f16_e32 v153, v228
	v_mul_f32_e32 v3, v135, v3
	v_cvt_f32_f16_e32 v135, v232
	v_mul_f32_e32 v37, v37, v3
	v_max_f32_e32 v3, 0x38d1b717, v153
	v_rcp_f32_e32 v3, v3
	v_max_f32_e32 v153, 0x38d1b717, v135
	v_cndmask_b32_e64 v135, v153, v135, s[0:1]
	v_cvt_f32_f16_sdwa v153, v228 dst_sel:DWORD dst_unused:UNUSED_PAD src0_sel:WORD_1
	v_mul_f32_e32 v3, v135, v3
	v_cvt_f32_f16_sdwa v135, v232 dst_sel:DWORD dst_unused:UNUSED_PAD src0_sel:WORD_1
	v_mul_f32_e32 v30, v30, v3
	v_max_f32_e32 v3, 0x38d1b717, v153
	v_rcp_f32_e32 v3, v3
	v_max_f32_e32 v153, 0x38d1b717, v135
	v_cndmask_b32_e64 v135, v153, v135, s[0:1]
	v_cvt_f32_f16_e32 v153, v229
	v_mul_f32_e32 v3, v135, v3
	v_cvt_f32_f16_e32 v135, v233
	v_mul_f32_e32 v31, v31, v3
	v_max_f32_e32 v3, 0x38d1b717, v153
	v_rcp_f32_e32 v3, v3
	v_max_f32_e32 v153, 0x38d1b717, v135
	v_cndmask_b32_e64 v135, v153, v135, s[0:1]
	v_cvt_f32_f16_sdwa v153, v229 dst_sel:DWORD dst_unused:UNUSED_PAD src0_sel:WORD_1
	v_mul_f32_e32 v3, v135, v3
	v_cvt_f32_f16_sdwa v135, v233 dst_sel:DWORD dst_unused:UNUSED_PAD src0_sel:WORD_1
	v_mul_f32_e32 v32, v32, v3
	v_max_f32_e32 v3, 0x38d1b717, v153
	v_rcp_f32_e32 v3, v3
	v_max_f32_e32 v153, 0x38d1b717, v135
	v_cndmask_b32_e64 v135, v153, v135, s[0:1]
	v_cvt_f32_f16_e32 v153, v234
	v_mul_f32_e32 v3, v135, v3
	v_cvt_f32_f16_e32 v135, v238
	v_mul_f32_e32 v33, v33, v3
	v_max_f32_e32 v3, 0x38d1b717, v153
	v_rcp_f32_e32 v3, v3
	v_max_f32_e32 v153, 0x38d1b717, v135
	v_cndmask_b32_e64 v135, v153, v135, s[0:1]
	v_cvt_f32_f16_sdwa v153, v234 dst_sel:DWORD dst_unused:UNUSED_PAD src0_sel:WORD_1
	v_mul_f32_e32 v3, v135, v3
	v_cvt_f32_f16_sdwa v135, v238 dst_sel:DWORD dst_unused:UNUSED_PAD src0_sel:WORD_1
	v_mul_f32_e32 v26, v26, v3
	v_max_f32_e32 v3, 0x38d1b717, v153
	v_rcp_f32_e32 v3, v3
	v_max_f32_e32 v153, 0x38d1b717, v135
	v_cndmask_b32_e64 v135, v153, v135, s[0:1]
	v_cvt_f32_f16_e32 v153, v235
	v_mul_f32_e32 v3, v135, v3
	v_cvt_f32_f16_e32 v135, v239
	v_mul_f32_e32 v27, v27, v3
	v_max_f32_e32 v3, 0x38d1b717, v153
	v_rcp_f32_e32 v3, v3
	v_max_f32_e32 v153, 0x38d1b717, v135
	v_cndmask_b32_e64 v135, v153, v135, s[0:1]
	v_cvt_f32_f16_sdwa v153, v235 dst_sel:DWORD dst_unused:UNUSED_PAD src0_sel:WORD_1
	v_mul_f32_e32 v3, v135, v3
	v_cvt_f32_f16_sdwa v135, v239 dst_sel:DWORD dst_unused:UNUSED_PAD src0_sel:WORD_1
	v_mul_f32_e32 v28, v28, v3
	v_max_f32_e32 v3, 0x38d1b717, v153
	v_rcp_f32_e32 v3, v3
	v_max_f32_e32 v153, 0x38d1b717, v135
	v_cndmask_b32_e64 v135, v153, v135, s[0:1]
	v_cvt_f32_f16_e32 v153, v236
	v_mul_f32_e32 v3, v135, v3
	v_cvt_f32_f16_e32 v135, v240
	v_mul_f32_e32 v29, v29, v3
	v_max_f32_e32 v3, 0x38d1b717, v153
	v_rcp_f32_e32 v3, v3
	v_max_f32_e32 v153, 0x38d1b717, v135
	v_cndmask_b32_e64 v135, v153, v135, s[0:1]
	v_cvt_f32_f16_sdwa v153, v236 dst_sel:DWORD dst_unused:UNUSED_PAD src0_sel:WORD_1
	v_mul_f32_e32 v3, v135, v3
	v_cvt_f32_f16_sdwa v135, v240 dst_sel:DWORD dst_unused:UNUSED_PAD src0_sel:WORD_1
	v_mul_f32_e32 v22, v22, v3
	v_max_f32_e32 v3, 0x38d1b717, v153
	v_rcp_f32_e32 v3, v3
	v_max_f32_e32 v153, 0x38d1b717, v135
	v_cndmask_b32_e64 v135, v153, v135, s[0:1]
	v_cvt_f32_f16_e32 v153, v237
	v_mul_f32_e32 v3, v135, v3
	v_cvt_f32_f16_e32 v135, v241
	v_mul_f32_e32 v23, v23, v3
	v_max_f32_e32 v3, 0x38d1b717, v153
	v_rcp_f32_e32 v3, v3
	v_cvt_f32_f16_sdwa v155, v237 dst_sel:DWORD dst_unused:UNUSED_PAD src0_sel:WORD_1
	v_max_f32_e32 v153, 0x38d1b717, v135
	v_cndmask_b32_e64 v135, v153, v135, s[0:1]
	v_mul_f32_e32 v3, v135, v3
	v_cvt_f32_f16_sdwa v135, v241 dst_sel:DWORD dst_unused:UNUSED_PAD src0_sel:WORD_1
	v_max_f32_e32 v153, 0x38d1b717, v155
	v_rcp_f32_e32 v153, v153
	v_mul_f32_e32 v24, v24, v3
	v_max_f32_e32 v3, 0x38d1b717, v135
	v_cndmask_b32_e64 v3, v3, v135, s[0:1]
	v_mul_f32_e32 v3, v3, v153
	v_mul_f32_e32 v25, v25, v3
	s_waitcnt vmcnt(0)
	v_cvt_f32_f16_e32 v3, v166
	v_cvt_f32_f16_e32 v4, v176
	v_max_f32_e32 v3, 0x38d1b717, v3
	v_rcp_f32_e32 v3, v3
	v_max_f32_e32 v5, 0x38d1b717, v4
	v_cndmask_b32_e64 v4, v5, v4, s[0:1]
	v_cvt_f32_f16_sdwa v5, v166 dst_sel:DWORD dst_unused:UNUSED_PAD src0_sel:WORD_1
	v_mul_f32_e32 v3, v4, v3
	v_cvt_f32_f16_sdwa v4, v176 dst_sel:DWORD dst_unused:UNUSED_PAD src0_sel:WORD_1
	v_mul_f32_e32 v18, v18, v3
	v_max_f32_e32 v3, 0x38d1b717, v5
	v_rcp_f32_e32 v3, v3
	v_max_f32_e32 v5, 0x38d1b717, v4
	v_cndmask_b32_e64 v4, v5, v4, s[0:1]
	v_cvt_f32_f16_e32 v5, v167
	v_mul_f32_e32 v3, v4, v3
	v_cvt_f32_f16_e32 v4, v177
	v_mul_f32_e32 v19, v19, v3
	v_max_f32_e32 v3, 0x38d1b717, v5
	v_rcp_f32_e32 v3, v3
	v_max_f32_e32 v5, 0x38d1b717, v4
	v_cndmask_b32_e64 v4, v5, v4, s[0:1]
	v_cvt_f32_f16_sdwa v5, v167 dst_sel:DWORD dst_unused:UNUSED_PAD src0_sel:WORD_1
	v_mul_f32_e32 v3, v4, v3
	v_cvt_f32_f16_sdwa v4, v177 dst_sel:DWORD dst_unused:UNUSED_PAD src0_sel:WORD_1
	v_mul_f32_e32 v20, v20, v3
	v_max_f32_e32 v3, 0x38d1b717, v5
	v_rcp_f32_e32 v3, v3
	v_max_f32_e32 v5, 0x38d1b717, v4
	v_cndmask_b32_e64 v4, v5, v4, s[0:1]
	v_cvt_f32_f16_e32 v5, v168
	v_mul_f32_e32 v3, v4, v3
	v_cvt_f32_f16_e32 v4, v178
	v_mul_f32_e32 v21, v21, v3
	v_max_f32_e32 v3, 0x38d1b717, v5
	v_rcp_f32_e32 v3, v3
	v_max_f32_e32 v5, 0x38d1b717, v4
	v_cndmask_b32_e64 v4, v5, v4, s[0:1]
	v_cvt_f32_f16_sdwa v5, v168 dst_sel:DWORD dst_unused:UNUSED_PAD src0_sel:WORD_1
	v_mul_f32_e32 v3, v4, v3
	v_cvt_f32_f16_sdwa v4, v178 dst_sel:DWORD dst_unused:UNUSED_PAD src0_sel:WORD_1
	v_mul_f32_e32 v14, v14, v3
	v_max_f32_e32 v3, 0x38d1b717, v5
	v_rcp_f32_e32 v3, v3
	v_max_f32_e32 v5, 0x38d1b717, v4
	v_cndmask_b32_e64 v4, v5, v4, s[0:1]
	v_cvt_f32_f16_e32 v5, v169
	v_mul_f32_e32 v3, v4, v3
	v_cvt_f32_f16_e32 v4, v179
	v_mul_f32_e32 v15, v15, v3
	v_max_f32_e32 v3, 0x38d1b717, v5
	v_rcp_f32_e32 v3, v3
	v_max_f32_e32 v5, 0x38d1b717, v4
	v_cndmask_b32_e64 v4, v5, v4, s[0:1]
	v_cvt_f32_f16_sdwa v5, v169 dst_sel:DWORD dst_unused:UNUSED_PAD src0_sel:WORD_1
	v_mul_f32_e32 v3, v4, v3
	v_cvt_f32_f16_sdwa v4, v179 dst_sel:DWORD dst_unused:UNUSED_PAD src0_sel:WORD_1
	v_mul_f32_e32 v16, v16, v3
	v_max_f32_e32 v3, 0x38d1b717, v5
	v_rcp_f32_e32 v3, v3
	v_max_f32_e32 v5, 0x38d1b717, v4
	v_cndmask_b32_e64 v4, v5, v4, s[0:1]
	v_cvt_f32_f16_e32 v5, v180
	v_mul_f32_e32 v3, v4, v3
	v_cvt_f32_f16_e32 v4, v184
	v_mul_f32_e32 v17, v17, v3
	v_max_f32_e32 v3, 0x38d1b717, v5
	v_rcp_f32_e32 v3, v3
	v_max_f32_e32 v5, 0x38d1b717, v4
	v_cndmask_b32_e64 v4, v5, v4, s[0:1]
	v_cvt_f32_f16_sdwa v5, v180 dst_sel:DWORD dst_unused:UNUSED_PAD src0_sel:WORD_1
	v_mul_f32_e32 v3, v4, v3
	v_cvt_f32_f16_sdwa v4, v184 dst_sel:DWORD dst_unused:UNUSED_PAD src0_sel:WORD_1
	v_mul_f32_e32 v10, v10, v3
	v_max_f32_e32 v3, 0x38d1b717, v5
	v_rcp_f32_e32 v3, v3
	v_max_f32_e32 v5, 0x38d1b717, v4
	v_cndmask_b32_e64 v4, v5, v4, s[0:1]
	v_cvt_f32_f16_e32 v5, v181
	v_mul_f32_e32 v3, v4, v3
	v_cvt_f32_f16_e32 v4, v185
	v_mul_f32_e32 v11, v11, v3
	v_max_f32_e32 v3, 0x38d1b717, v5
	v_rcp_f32_e32 v3, v3
	v_max_f32_e32 v5, 0x38d1b717, v4
	v_cndmask_b32_e64 v4, v5, v4, s[0:1]
	v_cvt_f32_f16_sdwa v5, v181 dst_sel:DWORD dst_unused:UNUSED_PAD src0_sel:WORD_1
	v_mul_f32_e32 v3, v4, v3
	v_cvt_f32_f16_sdwa v4, v185 dst_sel:DWORD dst_unused:UNUSED_PAD src0_sel:WORD_1
	v_mul_f32_e32 v12, v12, v3
	v_max_f32_e32 v3, 0x38d1b717, v5
	v_rcp_f32_e32 v3, v3
	v_max_f32_e32 v5, 0x38d1b717, v4
	v_cndmask_b32_e64 v4, v5, v4, s[0:1]
	v_cvt_f32_f16_e32 v5, v182
	v_mul_f32_e32 v3, v4, v3
	v_cvt_f32_f16_e32 v4, v186
	v_mul_f32_e32 v13, v13, v3
	v_max_f32_e32 v3, 0x38d1b717, v5
	v_rcp_f32_e32 v3, v3
	v_max_f32_e32 v5, 0x38d1b717, v4
	v_cndmask_b32_e64 v4, v5, v4, s[0:1]
	v_cvt_f32_f16_sdwa v5, v182 dst_sel:DWORD dst_unused:UNUSED_PAD src0_sel:WORD_1
	v_mul_f32_e32 v3, v4, v3
	v_cvt_f32_f16_sdwa v4, v186 dst_sel:DWORD dst_unused:UNUSED_PAD src0_sel:WORD_1
	v_mul_f32_e32 v6, v6, v3
	v_max_f32_e32 v3, 0x38d1b717, v5
	v_rcp_f32_e32 v3, v3
	v_max_f32_e32 v5, 0x38d1b717, v4
	v_cndmask_b32_e64 v4, v5, v4, s[0:1]
	v_cvt_f32_f16_e32 v5, v183
	v_mul_f32_e32 v3, v4, v3
	v_cvt_f32_f16_e32 v4, v187
	v_mul_f32_e32 v7, v7, v3
	v_max_f32_e32 v3, 0x38d1b717, v5
	v_rcp_f32_e32 v3, v3
	v_cvt_f32_f16_sdwa v135, v183 dst_sel:DWORD dst_unused:UNUSED_PAD src0_sel:WORD_1
	v_max_f32_e32 v5, 0x38d1b717, v4
	v_cndmask_b32_e64 v4, v5, v4, s[0:1]
	v_mul_f32_e32 v3, v4, v3
	v_cvt_f32_f16_sdwa v4, v187 dst_sel:DWORD dst_unused:UNUSED_PAD src0_sel:WORD_1
	v_max_f32_e32 v5, 0x38d1b717, v135
	v_rcp_f32_e32 v5, v5
	v_mul_f32_e32 v8, v8, v3
	v_max_f32_e32 v3, 0x38d1b717, v4
	v_cndmask_b32_e64 v3, v3, v4, s[0:1]
	v_mul_f32_e32 v3, v3, v5
	v_mul_f32_e32 v9, v9, v3
	s_branch .LBB0_5351
